# baseline (speedup 1.0000x reference)
.Lgsk_g3_0:
	v_fma_f32 v83, |v83|, v86, v83
	v_fma_f32 v88, |v88|, v91, v88
	v_fma_f32 v93, |v93|, v96, v93
	v_fma_f32 v98, |v98|, v101, v98
	v_cvt_f16_f32_e32 v82, v83
	v_cvt_f16_f32_e32 v87, v88
	v_cvt_f16_f32_e32 v92, v93
	v_cvt_f16_f32_e32 v97, v98
	v_cvt_f32_f16_e32 v84, v82
	v_cvt_f32_f16_e32 v89, v87
	v_cvt_f32_f16_e32 v94, v92
	v_cvt_f32_f16_e32 v99, v97
	v_sub_f32_e32 v84, v83, v84
	v_sub_f32_e32 v89, v88, v89
	v_sub_f32_e32 v94, v93, v94
	v_sub_f32_e32 v99, v98, v99
	v_cvt_f16_f32_e32 v84, v84
	v_cvt_f16_f32_e32 v89, v89
	v_cvt_f16_f32_e32 v94, v94
	v_cvt_f16_f32_e32 v99, v99
	ds_write_b16 v71, v82
	ds_write_b16 v71, v87 offset:144
	ds_write_b16 v71, v92 offset:288
	ds_write_b16 v71, v97 offset:432
	ds_write_b16 v71, v84 offset:4608
	ds_write_b16 v71, v89 offset:4752
	ds_write_b16 v71, v94 offset:4896
	ds_write_b16 v71, v99 offset:5040
	v_fma_f32 v82, v58, s61, v141
	v_fma_f32 v87, v59, s61, v141
	v_fma_f32 v92, v60, s61, v141
	v_fma_f32 v97, v61, s61, v141
	v_fma_f32 v83, v58, s62, v145
	v_fma_f32 v88, v59, s62, v145
	v_fma_f32 v93, v60, s62, v145
	v_fma_f32 v98, v61, s62, v145
	v_mul_f32_e32 v84, v82, v82
	v_mul_f32_e32 v89, v87, v87
	v_mul_f32_e32 v94, v92, v92
	v_mul_f32_e32 v99, v97, v97
	v_cmp_lt_f32_e64 s[64:65], |v82|, 1.0
	v_cmp_lt_f32_e64 s[66:67], |v87|, 1.0
	v_cmp_lt_f32_e64 s[68:69], |v92|, 1.0
	v_cmp_lt_f32_e64 s[70:71], |v97|, 1.0
	v_fma_f32 v86, v84, v103, s56
	v_fma_f32 v91, v89, v103, s56
	v_fma_f32 v96, v94, v103, s56
	v_fma_f32 v101, v99, v103, s56
	s_and_b64 s[72:73], s[64:65], s[66:67]
	s_and_b64 s[74:75], s[68:69], s[70:71]
	s_and_b64 s[72:73], s[72:73], s[74:75]
	v_fma_f32 v86, v84, v86, s57
	v_fma_f32 v91, v89, v91, s57
	v_fma_f32 v96, v94, v96, s57
	v_fma_f32 v101, v99, v101, s57
	v_fma_f32 v86, v84, v86, s58
	v_fma_f32 v91, v89, v91, s58
	v_fma_f32 v96, v94, v96, s58
	v_fma_f32 v101, v99, v101, s58
	v_fma_f32 v86, v84, v86, s59
	v_fma_f32 v91, v89, v91, s59
	v_fma_f32 v96, v94, v96, s59
	v_fma_f32 v101, v99, v101, s59
	v_fma_f32 v86, v84, v86, s60
	v_fma_f32 v91, v89, v91, s60
	v_fma_f32 v96, v94, v96, s60
	v_fma_f32 v101, v99, v101, s60
	v_fma_f32 v86, |v82|, v86, |v82|
	v_fma_f32 v91, |v87|, v91, |v87|
	v_fma_f32 v96, |v92|, v96, |v92|
	v_fma_f32 v101, |v97|, v101, |v97|
	s_cmp_eq_u64 s[72:73], exec
	s_cbranch_scc1 .Lgsk_g3_1
	v_fma_f32 v85, |v82|, v102, s50
	v_fma_f32 v90, |v87|, v102, s50
	v_fma_f32 v95, |v92|, v102, s50
	v_fma_f32 v100, |v97|, v102, s50
	v_fma_f32 v85, |v82|, v85, s51
	v_fma_f32 v90, |v87|, v90, s51
	v_fma_f32 v95, |v92|, v95, s51
	v_fma_f32 v100, |v97|, v100, s51
	v_fma_f32 v85, |v82|, v85, s52
	v_fma_f32 v90, |v87|, v90, s52
	v_fma_f32 v95, |v92|, v95, s52
	v_fma_f32 v100, |v97|, v100, s52
	v_fma_f32 v85, |v82|, v85, s53
	v_fma_f32 v90, |v87|, v90, s53
	v_fma_f32 v95, |v92|, v95, s53
	v_fma_f32 v100, |v97|, v100, s53
	v_fma_f32 v85, |v82|, v85, s54
	v_fma_f32 v90, |v87|, v90, s54
	v_fma_f32 v95, |v92|, v95, s54
	v_fma_f32 v100, |v97|, v100, s54
	v_fma_f32 v85, |v82|, v85, s55
	v_fma_f32 v90, |v87|, v90, s55
	v_fma_f32 v95, |v92|, v95, s55
	v_fma_f32 v100, |v97|, v100, s55
	v_fma_f32 v85, |v82|, v85, |v82|
	v_fma_f32 v90, |v87|, v90, |v87|
	v_fma_f32 v95, |v92|, v95, |v92|
	v_fma_f32 v100, |v97|, v100, |v97|
	v_mul_f32_e32 v85, 0xbfb8aa3b, v85
	v_mul_f32_e32 v90, 0xbfb8aa3b, v90
	v_mul_f32_e32 v95, 0xbfb8aa3b, v95
	v_mul_f32_e32 v100, 0xbfb8aa3b, v100
	v_exp_f32_e32 v85, v85
	v_exp_f32_e32 v90, v90
	v_exp_f32_e32 v95, v95
	v_exp_f32_e32 v100, v100
	s_nop 0
	v_sub_f32_e32 v85, 1.0, v85
	v_sub_f32_e32 v90, 1.0, v90
	v_sub_f32_e32 v95, 1.0, v95
	v_sub_f32_e32 v100, 1.0, v100
	v_cndmask_b32_e64 v86, v85, v86, s[64:65]
	v_cndmask_b32_e64 v91, v90, v91, s[66:67]
	v_cndmask_b32_e64 v96, v95, v96, s[68:69]
	v_cndmask_b32_e64 v101, v100, v101, s[70:71]
.Lgsk_g3_1:
	v_fma_f32 v83, |v83|, v86, v83
	v_fma_f32 v88, |v88|, v91, v88
	v_fma_f32 v93, |v93|, v96, v93
	v_fma_f32 v98, |v98|, v101, v98
	v_cvt_f16_f32_e32 v82, v83
	v_cvt_f16_f32_e32 v87, v88
	v_cvt_f16_f32_e32 v92, v93
	v_cvt_f16_f32_e32 v97, v98
	v_cvt_f32_f16_e32 v84, v82
	v_cvt_f32_f16_e32 v89, v87
	v_cvt_f32_f16_e32 v94, v92
	v_cvt_f32_f16_e32 v99, v97
	v_sub_f32_e32 v84, v83, v84
	v_sub_f32_e32 v89, v88, v89
	v_sub_f32_e32 v94, v93, v94
	v_sub_f32_e32 v99, v98, v99
	v_cvt_f16_f32_e32 v84, v84
	v_cvt_f16_f32_e32 v89, v89
	v_cvt_f16_f32_e32 v94, v94
	v_cvt_f16_f32_e32 v99, v99
	ds_write_b16 v71, v82 offset:32
	ds_write_b16 v71, v87 offset:176
	ds_write_b16 v71, v92 offset:320
	ds_write_b16 v71, v97 offset:464
	ds_write_b16 v71, v84 offset:4640
	ds_write_b16 v71, v89 offset:4784
	ds_write_b16 v71, v94 offset:4928
	ds_write_b16 v71, v99 offset:5072
	v_fma_f32 v82, v54, s61, v142
	v_fma_f32 v87, v55, s61, v142
	v_fma_f32 v92, v56, s61, v142
	v_fma_f32 v97, v57, s61, v142
	v_fma_f32 v83, v54, s62, v146
	v_fma_f32 v88, v55, s62, v146
	v_fma_f32 v93, v56, s62, v146
	v_fma_f32 v98, v57, s62, v146
	v_mul_f32_e32 v84, v82, v82
	v_mul_f32_e32 v89, v87, v87
	v_mul_f32_e32 v94, v92, v92
	v_mul_f32_e32 v99, v97, v97
	v_cmp_lt_f32_e64 s[64:65], |v82|, 1.0
	v_cmp_lt_f32_e64 s[66:67], |v87|, 1.0
	v_cmp_lt_f32_e64 s[68:69], |v92|, 1.0
	v_cmp_lt_f32_e64 s[70:71], |v97|, 1.0
	v_fma_f32 v86, v84, v103, s56
	v_fma_f32 v91, v89, v103, s56
	v_fma_f32 v96, v94, v103, s56
	v_fma_f32 v101, v99, v103, s56
	s_and_b64 s[72:73], s[64:65], s[66:67]
	s_and_b64 s[74:75], s[68:69], s[70:71]
	s_and_b64 s[72:73], s[72:73], s[74:75]
	v_fma_f32 v86, v84, v86, s57
	v_fma_f32 v91, v89, v91, s57
	v_fma_f32 v96, v94, v96, s57
	v_fma_f32 v101, v99, v101, s57
	v_fma_f32 v86, v84, v86, s58
	v_fma_f32 v91, v89, v91, s58
	v_fma_f32 v96, v94, v96, s58
	v_fma_f32 v101, v99, v101, s58
	v_fma_f32 v86, v84, v86, s59
	v_fma_f32 v91, v89, v91, s59
	v_fma_f32 v96, v94, v96, s59
	v_fma_f32 v101, v99, v101, s59
	v_fma_f32 v86, v84, v86, s60
	v_fma_f32 v91, v89, v91, s60
	v_fma_f32 v96, v94, v96, s60
	v_fma_f32 v101, v99, v101, s60
	v_fma_f32 v86, |v82|, v86, |v82|
	v_fma_f32 v91, |v87|, v91, |v87|
	v_fma_f32 v96, |v92|, v96, |v92|
	v_fma_f32 v101, |v97|, v101, |v97|
	s_cmp_eq_u64 s[72:73], exec
	s_cbranch_scc1 .Lgsk_g3_2
	v_fma_f32 v85, |v82|, v102, s50
	v_fma_f32 v90, |v87|, v102, s50
	v_fma_f32 v95, |v92|, v102, s50
	v_fma_f32 v100, |v97|, v102, s50
	v_fma_f32 v85, |v82|, v85, s51
	v_fma_f32 v90, |v87|, v90, s51
	v_fma_f32 v95, |v92|, v95, s51
	v_fma_f32 v100, |v97|, v100, s51
	v_fma_f32 v85, |v82|, v85, s52
	v_fma_f32 v90, |v87|, v90, s52
	v_fma_f32 v95, |v92|, v95, s52
	v_fma_f32 v100, |v97|, v100, s52
	v_fma_f32 v85, |v82|, v85, s53
	v_fma_f32 v90, |v87|, v90, s53
	v_fma_f32 v95, |v92|, v95, s53
	v_fma_f32 v100, |v97|, v100, s53
	v_fma_f32 v85, |v82|, v85, s54
	v_fma_f32 v90, |v87|, v90, s54
	v_fma_f32 v95, |v92|, v95, s54
	v_fma_f32 v100, |v97|, v100, s54
	v_fma_f32 v85, |v82|, v85, s55
	v_fma_f32 v90, |v87|, v90, s55
	v_fma_f32 v95, |v92|, v95, s55
	v_fma_f32 v100, |v97|, v100, s55
	v_fma_f32 v85, |v82|, v85, |v82|
	v_fma_f32 v90, |v87|, v90, |v87|
	v_fma_f32 v95, |v92|, v95, |v92|
	v_fma_f32 v100, |v97|, v100, |v97|
	v_mul_f32_e32 v85, 0xbfb8aa3b, v85
	v_mul_f32_e32 v90, 0xbfb8aa3b, v90
	v_mul_f32_e32 v95, 0xbfb8aa3b, v95
	v_mul_f32_e32 v100, 0xbfb8aa3b, v100
	v_exp_f32_e32 v85, v85
	v_exp_f32_e32 v90, v90
	v_exp_f32_e32 v95, v95
	v_exp_f32_e32 v100, v100
	s_nop 0
	v_sub_f32_e32 v85, 1.0, v85
	v_sub_f32_e32 v90, 1.0, v90
	v_sub_f32_e32 v95, 1.0, v95
	v_sub_f32_e32 v100, 1.0, v100
	v_cndmask_b32_e64 v86, v85, v86, s[64:65]
	v_cndmask_b32_e64 v91, v90, v91, s[66:67]
	v_cndmask_b32_e64 v96, v95, v96, s[68:69]
	v_cndmask_b32_e64 v101, v100, v101, s[70:71]
.Lgsk_g3_2:
	v_fma_f32 v83, |v83|, v86, v83
	v_fma_f32 v88, |v88|, v91, v88
	v_fma_f32 v93, |v93|, v96, v93
	v_fma_f32 v98, |v98|, v101, v98
	v_cvt_f16_f32_e32 v82, v83
	v_cvt_f16_f32_e32 v87, v88
	v_cvt_f16_f32_e32 v92, v93
	v_cvt_f16_f32_e32 v97, v98
	v_cvt_f32_f16_e32 v84, v82
	v_cvt_f32_f16_e32 v89, v87
	v_cvt_f32_f16_e32 v94, v92
	v_cvt_f32_f16_e32 v99, v97
	v_sub_f32_e32 v84, v83, v84
	v_sub_f32_e32 v89, v88, v89
	v_sub_f32_e32 v94, v93, v94
	v_sub_f32_e32 v99, v98, v99
	v_cvt_f16_f32_e32 v84, v84
	v_cvt_f16_f32_e32 v89, v89
	v_cvt_f16_f32_e32 v94, v94
	v_cvt_f16_f32_e32 v99, v99
	ds_write_b16 v71, v82 offset:64
	ds_write_b16 v71, v87 offset:208
	ds_write_b16 v71, v92 offset:352
	ds_write_b16 v71, v97 offset:496
	ds_write_b16 v71, v84 offset:4672
	ds_write_b16 v71, v89 offset:4816
	ds_write_b16 v71, v94 offset:4960
	ds_write_b16 v71, v99 offset:5104
	v_fma_f32 v82, v50, s61, v143
	v_fma_f32 v87, v51, s61, v143
	v_fma_f32 v92, v52, s61, v143
	v_fma_f32 v97, v53, s61, v143
	v_fma_f32 v83, v50, s62, v147
	v_fma_f32 v88, v51, s62, v147
	v_fma_f32 v93, v52, s62, v147
	v_fma_f32 v98, v53, s62, v147
	v_mul_f32_e32 v84, v82, v82
	v_mul_f32_e32 v89, v87, v87
	v_mul_f32_e32 v94, v92, v92
	v_mul_f32_e32 v99, v97, v97
	v_cmp_lt_f32_e64 s[64:65], |v82|, 1.0
	v_cmp_lt_f32_e64 s[66:67], |v87|, 1.0
	v_cmp_lt_f32_e64 s[68:69], |v92|, 1.0
	v_cmp_lt_f32_e64 s[70:71], |v97|, 1.0
	v_fma_f32 v86, v84, v103, s56
	v_fma_f32 v91, v89, v103, s56
	v_fma_f32 v96, v94, v103, s56
	v_fma_f32 v101, v99, v103, s56
	s_and_b64 s[72:73], s[64:65], s[66:67]
	s_and_b64 s[74:75], s[68:69], s[70:71]
	s_and_b64 s[72:73], s[72:73], s[74:75]
	v_fma_f32 v86, v84, v86, s57
	v_fma_f32 v91, v89, v91, s57
	v_fma_f32 v96, v94, v96, s57
	v_fma_f32 v101, v99, v101, s57
	v_fma_f32 v86, v84, v86, s58
	v_fma_f32 v91, v89, v91, s58
	v_fma_f32 v96, v94, v96, s58
	v_fma_f32 v101, v99, v101, s58
	v_fma_f32 v86, v84, v86, s59
	v_fma_f32 v91, v89, v91, s59
	v_fma_f32 v96, v94, v96, s59
	v_fma_f32 v101, v99, v101, s59
	v_fma_f32 v86, v84, v86, s60
	v_fma_f32 v91, v89, v91, s60
	v_fma_f32 v96, v94, v96, s60
	v_fma_f32 v101, v99, v101, s60
	v_fma_f32 v86, |v82|, v86, |v82|
	v_fma_f32 v91, |v87|, v91, |v87|
	v_fma_f32 v96, |v92|, v96, |v92|
	v_fma_f32 v101, |v97|, v101, |v97|
	s_cmp_eq_u64 s[72:73], exec
	s_cbranch_scc1 .Lgsk_g3_3
	v_fma_f32 v85, |v82|, v102, s50
	v_fma_f32 v90, |v87|, v102, s50
	v_fma_f32 v95, |v92|, v102, s50
	v_fma_f32 v100, |v97|, v102, s50
	v_fma_f32 v85, |v82|, v85, s51
	v_fma_f32 v90, |v87|, v90, s51
	v_fma_f32 v95, |v92|, v95, s51
	v_fma_f32 v100, |v97|, v100, s51
	v_fma_f32 v85, |v82|, v85, s52
	v_fma_f32 v90, |v87|, v90, s52
	v_fma_f32 v95, |v92|, v95, s52
	v_fma_f32 v100, |v97|, v100, s52
	v_fma_f32 v85, |v82|, v85, s53
	v_fma_f32 v90, |v87|, v90, s53
	v_fma_f32 v95, |v92|, v95, s53
	v_fma_f32 v100, |v97|, v100, s53
	v_fma_f32 v85, |v82|, v85, s54
	v_fma_f32 v90, |v87|, v90, s54
	v_fma_f32 v95, |v92|, v95, s54
	v_fma_f32 v100, |v97|, v100, s54
	v_fma_f32 v85, |v82|, v85, s55
	v_fma_f32 v90, |v87|, v90, s55
	v_fma_f32 v95, |v92|, v95, s55
	v_fma_f32 v100, |v97|, v100, s55
	v_fma_f32 v85, |v82|, v85, |v82|
	v_fma_f32 v90, |v87|, v90, |v87|
	v_fma_f32 v95, |v92|, v95, |v92|
	v_fma_f32 v100, |v97|, v100, |v97|
	v_mul_f32_e32 v85, 0xbfb8aa3b, v85
	v_mul_f32_e32 v90, 0xbfb8aa3b, v90
	v_mul_f32_e32 v95, 0xbfb8aa3b, v95
	v_mul_f32_e32 v100, 0xbfb8aa3b, v100
	v_exp_f32_e32 v85, v85
	v_exp_f32_e32 v90, v90
	v_exp_f32_e32 v95, v95
	v_exp_f32_e32 v100, v100
	s_nop 0
	v_sub_f32_e32 v85, 1.0, v85
	v_sub_f32_e32 v90, 1.0, v90
	v_sub_f32_e32 v95, 1.0, v95
	v_sub_f32_e32 v100, 1.0, v100
	v_cndmask_b32_e64 v86, v85, v86, s[64:65]
	v_cndmask_b32_e64 v91, v90, v91, s[66:67]
	v_cndmask_b32_e64 v96, v95, v96, s[68:69]
	v_cndmask_b32_e64 v101, v100, v101, s[70:71]
.Lgsk_g3_3:
	v_fma_f32 v83, |v83|, v86, v83
	v_fma_f32 v88, |v88|, v91, v88
	v_fma_f32 v93, |v93|, v96, v93
	v_fma_f32 v98, |v98|, v101, v98
	v_cvt_f16_f32_e32 v82, v83
	v_cvt_f16_f32_e32 v87, v88
	v_cvt_f16_f32_e32 v92, v93
	v_cvt_f16_f32_e32 v97, v98
	v_cvt_f32_f16_e32 v84, v82
	v_cvt_f32_f16_e32 v89, v87
	v_cvt_f32_f16_e32 v94, v92
	v_cvt_f32_f16_e32 v99, v97
	v_sub_f32_e32 v84, v83, v84
	v_sub_f32_e32 v89, v88, v89
	v_sub_f32_e32 v94, v93, v94
	v_sub_f32_e32 v99, v98, v99
	v_cvt_f16_f32_e32 v84, v84
	v_cvt_f16_f32_e32 v89, v89
	v_cvt_f16_f32_e32 v94, v94
	v_cvt_f16_f32_e32 v99, v99
	ds_write_b16 v71, v82 offset:96
	ds_write_b16 v71, v87 offset:240
	ds_write_b16 v71, v92 offset:384
	ds_write_b16 v71, v97 offset:528
	ds_write_b16 v71, v84 offset:4704
	ds_write_b16 v71, v89 offset:4848
	ds_write_b16 v71, v94 offset:4992
	ds_write_b16 v71, v99 offset:5136
	v_fma_f32 v82, v46, s61, v140
	v_fma_f32 v87, v47, s61, v140
	v_fma_f32 v92, v48, s61, v140
	v_fma_f32 v97, v49, s61, v140
	v_fma_f32 v83, v46, s62, v144
	v_fma_f32 v88, v47, s62, v144
	v_fma_f32 v93, v48, s62, v144
	v_fma_f32 v98, v49, s62, v144
	v_mul_f32_e32 v84, v82, v82
	v_mul_f32_e32 v89, v87, v87
	v_mul_f32_e32 v94, v92, v92
	v_mul_f32_e32 v99, v97, v97
	v_cmp_lt_f32_e64 s[64:65], |v82|, 1.0
	v_cmp_lt_f32_e64 s[66:67], |v87|, 1.0
	v_cmp_lt_f32_e64 s[68:69], |v92|, 1.0
	v_cmp_lt_f32_e64 s[70:71], |v97|, 1.0
	v_fma_f32 v86, v84, v103, s56
	v_fma_f32 v91, v89, v103, s56
	v_fma_f32 v96, v94, v103, s56
	v_fma_f32 v101, v99, v103, s56
	s_and_b64 s[72:73], s[64:65], s[66:67]
	s_and_b64 s[74:75], s[68:69], s[70:71]
	s_and_b64 s[72:73], s[72:73], s[74:75]
	v_fma_f32 v86, v84, v86, s57
	v_fma_f32 v91, v89, v91, s57
	v_fma_f32 v96, v94, v96, s57
	v_fma_f32 v101, v99, v101, s57
	v_fma_f32 v86, v84, v86, s58
	v_fma_f32 v91, v89, v91, s58
	v_fma_f32 v96, v94, v96, s58
	v_fma_f32 v101, v99, v101, s58
	v_fma_f32 v86, v84, v86, s59
	v_fma_f32 v91, v89, v91, s59
	v_fma_f32 v96, v94, v96, s59
	v_fma_f32 v101, v99, v101, s59
	v_fma_f32 v86, v84, v86, s60
	v_fma_f32 v91, v89, v91, s60
	v_fma_f32 v96, v94, v96, s60
	v_fma_f32 v101, v99, v101, s60
	v_fma_f32 v86, |v82|, v86, |v82|
	v_fma_f32 v91, |v87|, v91, |v87|
	v_fma_f32 v96, |v92|, v96, |v92|
	v_fma_f32 v101, |v97|, v101, |v97|
	s_cmp_eq_u64 s[72:73], exec
	s_cbranch_scc1 .Lgsk_g3_4
	v_fma_f32 v85, |v82|, v102, s50
	v_fma_f32 v90, |v87|, v102, s50
	v_fma_f32 v95, |v92|, v102, s50
	v_fma_f32 v100, |v97|, v102, s50
	v_fma_f32 v85, |v82|, v85, s51
	v_fma_f32 v90, |v87|, v90, s51
	v_fma_f32 v95, |v92|, v95, s51
	v_fma_f32 v100, |v97|, v100, s51
	v_fma_f32 v85, |v82|, v85, s52
	v_fma_f32 v90, |v87|, v90, s52
	v_fma_f32 v95, |v92|, v95, s52
	v_fma_f32 v100, |v97|, v100, s52
	v_fma_f32 v85, |v82|, v85, s53
	v_fma_f32 v90, |v87|, v90, s53
	v_fma_f32 v95, |v92|, v95, s53
	v_fma_f32 v100, |v97|, v100, s53
	v_fma_f32 v85, |v82|, v85, s54
	v_fma_f32 v90, |v87|, v90, s54
	v_fma_f32 v95, |v92|, v95, s54
	v_fma_f32 v100, |v97|, v100, s54
	v_fma_f32 v85, |v82|, v85, s55
	v_fma_f32 v90, |v87|, v90, s55
	v_fma_f32 v95, |v92|, v95, s55
	v_fma_f32 v100, |v97|, v100, s55
	v_fma_f32 v85, |v82|, v85, |v82|
	v_fma_f32 v90, |v87|, v90, |v87|
	v_fma_f32 v95, |v92|, v95, |v92|
	v_fma_f32 v100, |v97|, v100, |v97|
	v_mul_f32_e32 v85, 0xbfb8aa3b, v85
	v_mul_f32_e32 v90, 0xbfb8aa3b, v90
	v_mul_f32_e32 v95, 0xbfb8aa3b, v95
	v_mul_f32_e32 v100, 0xbfb8aa3b, v100
	v_exp_f32_e32 v85, v85
	v_exp_f32_e32 v90, v90
	v_exp_f32_e32 v95, v95
	v_exp_f32_e32 v100, v100
	s_nop 0
	v_sub_f32_e32 v85, 1.0, v85
	v_sub_f32_e32 v90, 1.0, v90
	v_sub_f32_e32 v95, 1.0, v95
	v_sub_f32_e32 v100, 1.0, v100
	v_cndmask_b32_e64 v86, v85, v86, s[64:65]
	v_cndmask_b32_e64 v91, v90, v91, s[66:67]
	v_cndmask_b32_e64 v96, v95, v96, s[68:69]
	v_cndmask_b32_e64 v101, v100, v101, s[70:71]
.Lgsk_g3_4:
	v_fma_f32 v83, |v83|, v86, v83
	v_fma_f32 v88, |v88|, v91, v88
	v_fma_f32 v93, |v93|, v96, v93
	v_fma_f32 v98, |v98|, v101, v98
	v_cvt_f16_f32_e32 v82, v83
	v_cvt_f16_f32_e32 v87, v88
	v_cvt_f16_f32_e32 v92, v93
	v_cvt_f16_f32_e32 v97, v98
	v_cvt_f32_f16_e32 v84, v82
	v_cvt_f32_f16_e32 v89, v87
	v_cvt_f32_f16_e32 v94, v92
	v_cvt_f32_f16_e32 v99, v97
	v_sub_f32_e32 v84, v83, v84
	v_sub_f32_e32 v89, v88, v89
	v_sub_f32_e32 v94, v93, v94
	v_sub_f32_e32 v99, v98, v99
	v_cvt_f16_f32_e32 v84, v84
	v_cvt_f16_f32_e32 v89, v89
	v_cvt_f16_f32_e32 v94, v94
	v_cvt_f16_f32_e32 v99, v99
	ds_write_b16 v71, v82 offset:2304
	ds_write_b16 v71, v87 offset:2448
	ds_write_b16 v71, v92 offset:2592
	ds_write_b16 v71, v97 offset:2736
	ds_write_b16 v71, v84 offset:6912
	ds_write_b16 v71, v89 offset:7056
	ds_write_b16 v71, v94 offset:7200
	ds_write_b16 v71, v99 offset:7344
	v_fma_f32 v82, v42, s61, v141
	v_fma_f32 v87, v43, s61, v141
	v_fma_f32 v92, v44, s61, v141
	v_fma_f32 v97, v45, s61, v141
	v_fma_f32 v83, v42, s62, v145
	v_fma_f32 v88, v43, s62, v145
	v_fma_f32 v93, v44, s62, v145
	v_fma_f32 v98, v45, s62, v145
	v_mul_f32_e32 v84, v82, v82
	v_mul_f32_e32 v89, v87, v87
	v_mul_f32_e32 v94, v92, v92
	v_mul_f32_e32 v99, v97, v97
	v_cmp_lt_f32_e64 s[64:65], |v82|, 1.0
	v_cmp_lt_f32_e64 s[66:67], |v87|, 1.0
	v_cmp_lt_f32_e64 s[68:69], |v92|, 1.0
	v_cmp_lt_f32_e64 s[70:71], |v97|, 1.0
	v_fma_f32 v86, v84, v103, s56
	v_fma_f32 v91, v89, v103, s56
	v_fma_f32 v96, v94, v103, s56
	v_fma_f32 v101, v99, v103, s56
	s_and_b64 s[72:73], s[64:65], s[66:67]
	s_and_b64 s[74:75], s[68:69], s[70:71]
	s_and_b64 s[72:73], s[72:73], s[74:75]
	v_fma_f32 v86, v84, v86, s57
	v_fma_f32 v91, v89, v91, s57
	v_fma_f32 v96, v94, v96, s57
	v_fma_f32 v101, v99, v101, s57
	v_fma_f32 v86, v84, v86, s58
	v_fma_f32 v91, v89, v91, s58
	v_fma_f32 v96, v94, v96, s58
	v_fma_f32 v101, v99, v101, s58
	v_fma_f32 v86, v84, v86, s59
	v_fma_f32 v91, v89, v91, s59
	v_fma_f32 v96, v94, v96, s59
	v_fma_f32 v101, v99, v101, s59
	v_fma_f32 v86, v84, v86, s60
	v_fma_f32 v91, v89, v91, s60
	v_fma_f32 v96, v94, v96, s60
	v_fma_f32 v101, v99, v101, s60
	v_fma_f32 v86, |v82|, v86, |v82|
	v_fma_f32 v91, |v87|, v91, |v87|
	v_fma_f32 v96, |v92|, v96, |v92|
	v_fma_f32 v101, |v97|, v101, |v97|
	s_cmp_eq_u64 s[72:73], exec
	s_cbranch_scc1 .Lgsk_g3_5
	v_fma_f32 v85, |v82|, v102, s50
	v_fma_f32 v90, |v87|, v102, s50
	v_fma_f32 v95, |v92|, v102, s50
	v_fma_f32 v100, |v97|, v102, s50
	v_fma_f32 v85, |v82|, v85, s51
	v_fma_f32 v90, |v87|, v90, s51
	v_fma_f32 v95, |v92|, v95, s51
	v_fma_f32 v100, |v97|, v100, s51
	v_fma_f32 v85, |v82|, v85, s52
	v_fma_f32 v90, |v87|, v90, s52
	v_fma_f32 v95, |v92|, v95, s52
	v_fma_f32 v100, |v97|, v100, s52
	v_fma_f32 v85, |v82|, v85, s53
	v_fma_f32 v90, |v87|, v90, s53
	v_fma_f32 v95, |v92|, v95, s53
	v_fma_f32 v100, |v97|, v100, s53
	v_fma_f32 v85, |v82|, v85, s54
	v_fma_f32 v90, |v87|, v90, s54
	v_fma_f32 v95, |v92|, v95, s54
	v_fma_f32 v100, |v97|, v100, s54
	v_fma_f32 v85, |v82|, v85, s55
	v_fma_f32 v90, |v87|, v90, s55
	v_fma_f32 v95, |v92|, v95, s55
	v_fma_f32 v100, |v97|, v100, s55
	v_fma_f32 v85, |v82|, v85, |v82|
	v_fma_f32 v90, |v87|, v90, |v87|
	v_fma_f32 v95, |v92|, v95, |v92|
	v_fma_f32 v100, |v97|, v100, |v97|
	v_mul_f32_e32 v85, 0xbfb8aa3b, v85
	v_mul_f32_e32 v90, 0xbfb8aa3b, v90
	v_mul_f32_e32 v95, 0xbfb8aa3b, v95
	v_mul_f32_e32 v100, 0xbfb8aa3b, v100
	v_exp_f32_e32 v85, v85
	v_exp_f32_e32 v90, v90
	v_exp_f32_e32 v95, v95
	v_exp_f32_e32 v100, v100
	s_nop 0
	v_sub_f32_e32 v85, 1.0, v85
	v_sub_f32_e32 v90, 1.0, v90
	v_sub_f32_e32 v95, 1.0, v95
	v_sub_f32_e32 v100, 1.0, v100
	v_cndmask_b32_e64 v86, v85, v86, s[64:65]
	v_cndmask_b32_e64 v91, v90, v91, s[66:67]
	v_cndmask_b32_e64 v96, v95, v96, s[68:69]
	v_cndmask_b32_e64 v101, v100, v101, s[70:71]
.Lgsk_g3_5:
	v_fma_f32 v83, |v83|, v86, v83
	v_fma_f32 v88, |v88|, v91, v88
	v_fma_f32 v93, |v93|, v96, v93
	v_fma_f32 v98, |v98|, v101, v98
	v_cvt_f16_f32_e32 v82, v83
	v_cvt_f16_f32_e32 v87, v88
	v_cvt_f16_f32_e32 v92, v93
	v_cvt_f16_f32_e32 v97, v98
	v_cvt_f32_f16_e32 v84, v82
	v_cvt_f32_f16_e32 v89, v87
	v_cvt_f32_f16_e32 v94, v92
	v_cvt_f32_f16_e32 v99, v97
	v_sub_f32_e32 v84, v83, v84
	v_sub_f32_e32 v89, v88, v89
	v_sub_f32_e32 v94, v93, v94
	v_sub_f32_e32 v99, v98, v99
	v_cvt_f16_f32_e32 v84, v84
	v_cvt_f16_f32_e32 v89, v89
	v_cvt_f16_f32_e32 v94, v94
	v_cvt_f16_f32_e32 v99, v99
	ds_write_b16 v71, v82 offset:2336
	ds_write_b16 v71, v87 offset:2480
	ds_write_b16 v71, v92 offset:2624
	ds_write_b16 v71, v97 offset:2768
	ds_write_b16 v71, v84 offset:6944
	ds_write_b16 v71, v89 offset:7088
	ds_write_b16 v71, v94 offset:7232
	ds_write_b16 v71, v99 offset:7376
	v_fma_f32 v82, v38, s61, v142
	v_fma_f32 v87, v39, s61, v142
	v_fma_f32 v92, v40, s61, v142
	v_fma_f32 v97, v41, s61, v142
	v_fma_f32 v83, v38, s62, v146
	v_fma_f32 v88, v39, s62, v146
	v_fma_f32 v93, v40, s62, v146
	v_fma_f32 v98, v41, s62, v146
	v_mul_f32_e32 v84, v82, v82
	v_mul_f32_e32 v89, v87, v87
	v_mul_f32_e32 v94, v92, v92
	v_mul_f32_e32 v99, v97, v97
	v_cmp_lt_f32_e64 s[64:65], |v82|, 1.0
	v_cmp_lt_f32_e64 s[66:67], |v87|, 1.0
	v_cmp_lt_f32_e64 s[68:69], |v92|, 1.0
	v_cmp_lt_f32_e64 s[70:71], |v97|, 1.0
	v_fma_f32 v86, v84, v103, s56
	v_fma_f32 v91, v89, v103, s56
	v_fma_f32 v96, v94, v103, s56
	v_fma_f32 v101, v99, v103, s56
	s_and_b64 s[72:73], s[64:65], s[66:67]
	s_and_b64 s[74:75], s[68:69], s[70:71]
	s_and_b64 s[72:73], s[72:73], s[74:75]
	v_fma_f32 v86, v84, v86, s57
	v_fma_f32 v91, v89, v91, s57
	v_fma_f32 v96, v94, v96, s57
	v_fma_f32 v101, v99, v101, s57
	v_fma_f32 v86, v84, v86, s58
	v_fma_f32 v91, v89, v91, s58
	v_fma_f32 v96, v94, v96, s58
	v_fma_f32 v101, v99, v101, s58
	v_fma_f32 v86, v84, v86, s59
	v_fma_f32 v91, v89, v91, s59
	v_fma_f32 v96, v94, v96, s59
	v_fma_f32 v101, v99, v101, s59
	v_fma_f32 v86, v84, v86, s60
	v_fma_f32 v91, v89, v91, s60
	v_fma_f32 v96, v94, v96, s60
	v_fma_f32 v101, v99, v101, s60
	v_fma_f32 v86, |v82|, v86, |v82|
	v_fma_f32 v91, |v87|, v91, |v87|
	v_fma_f32 v96, |v92|, v96, |v92|
	v_fma_f32 v101, |v97|, v101, |v97|
	s_cmp_eq_u64 s[72:73], exec
	s_cbranch_scc1 .Lgsk_g3_6
	v_fma_f32 v85, |v82|, v102, s50
	v_fma_f32 v90, |v87|, v102, s50
	v_fma_f32 v95, |v92|, v102, s50
	v_fma_f32 v100, |v97|, v102, s50
	v_fma_f32 v85, |v82|, v85, s51
	v_fma_f32 v90, |v87|, v90, s51
	v_fma_f32 v95, |v92|, v95, s51
	v_fma_f32 v100, |v97|, v100, s51
	v_fma_f32 v85, |v82|, v85, s52
	v_fma_f32 v90, |v87|, v90, s52
	v_fma_f32 v95, |v92|, v95, s52
	v_fma_f32 v100, |v97|, v100, s52
	v_fma_f32 v85, |v82|, v85, s53
	v_fma_f32 v90, |v87|, v90, s53
	v_fma_f32 v95, |v92|, v95, s53
	v_fma_f32 v100, |v97|, v100, s53
	v_fma_f32 v85, |v82|, v85, s54
	v_fma_f32 v90, |v87|, v90, s54
	v_fma_f32 v95, |v92|, v95, s54
	v_fma_f32 v100, |v97|, v100, s54
	v_fma_f32 v85, |v82|, v85, s55
	v_fma_f32 v90, |v87|, v90, s55
	v_fma_f32 v95, |v92|, v95, s55
	v_fma_f32 v100, |v97|, v100, s55
	v_fma_f32 v85, |v82|, v85, |v82|
	v_fma_f32 v90, |v87|, v90, |v87|
	v_fma_f32 v95, |v92|, v95, |v92|
	v_fma_f32 v100, |v97|, v100, |v97|
	v_mul_f32_e32 v85, 0xbfb8aa3b, v85
	v_mul_f32_e32 v90, 0xbfb8aa3b, v90
	v_mul_f32_e32 v95, 0xbfb8aa3b, v95
	v_mul_f32_e32 v100, 0xbfb8aa3b, v100
	v_exp_f32_e32 v85, v85
	v_exp_f32_e32 v90, v90
	v_exp_f32_e32 v95, v95
	v_exp_f32_e32 v100, v100
	s_nop 0
	v_sub_f32_e32 v85, 1.0, v85
	v_sub_f32_e32 v90, 1.0, v90
	v_sub_f32_e32 v95, 1.0, v95
	v_sub_f32_e32 v100, 1.0, v100
	v_cndmask_b32_e64 v86, v85, v86, s[64:65]
	v_cndmask_b32_e64 v91, v90, v91, s[66:67]
	v_cndmask_b32_e64 v96, v95, v96, s[68:69]
	v_cndmask_b32_e64 v101, v100, v101, s[70:71]
.Lgsk_g3_6:
	v_fma_f32 v83, |v83|, v86, v83
	v_fma_f32 v88, |v88|, v91, v88
	v_fma_f32 v93, |v93|, v96, v93
	v_fma_f32 v98, |v98|, v101, v98
	v_cvt_f16_f32_e32 v82, v83
	v_cvt_f16_f32_e32 v87, v88
	v_cvt_f16_f32_e32 v92, v93
	v_cvt_f16_f32_e32 v97, v98
	v_cvt_f32_f16_e32 v84, v82
	v_cvt_f32_f16_e32 v89, v87
	v_cvt_f32_f16_e32 v94, v92
	v_cvt_f32_f16_e32 v99, v97
	v_sub_f32_e32 v84, v83, v84
	v_sub_f32_e32 v89, v88, v89
	v_sub_f32_e32 v94, v93, v94
	v_sub_f32_e32 v99, v98, v99
	v_cvt_f16_f32_e32 v84, v84
	v_cvt_f16_f32_e32 v89, v89
	v_cvt_f16_f32_e32 v94, v94
	v_cvt_f16_f32_e32 v99, v99
	ds_write_b16 v71, v82 offset:2368
	ds_write_b16 v71, v87 offset:2512
	ds_write_b16 v71, v92 offset:2656
	ds_write_b16 v71, v97 offset:2800
	ds_write_b16 v71, v84 offset:6976
	ds_write_b16 v71, v89 offset:7120
	ds_write_b16 v71, v94 offset:7264
	ds_write_b16 v71, v99 offset:7408
	v_fma_f32 v82, v34, s61, v143
	v_fma_f32 v87, v35, s61, v143
	v_fma_f32 v92, v36, s61, v143
	v_fma_f32 v97, v37, s61, v143
	v_fma_f32 v83, v34, s62, v147
	v_fma_f32 v88, v35, s62, v147
	v_fma_f32 v93, v36, s62, v147
	v_fma_f32 v98, v37, s62, v147
	v_mul_f32_e32 v84, v82, v82
	v_mul_f32_e32 v89, v87, v87
	v_mul_f32_e32 v94, v92, v92
	v_mul_f32_e32 v99, v97, v97
	v_cmp_lt_f32_e64 s[64:65], |v82|, 1.0
	v_cmp_lt_f32_e64 s[66:67], |v87|, 1.0
	v_cmp_lt_f32_e64 s[68:69], |v92|, 1.0
	v_cmp_lt_f32_e64 s[70:71], |v97|, 1.0
	v_fma_f32 v86, v84, v103, s56
	v_fma_f32 v91, v89, v103, s56
	v_fma_f32 v96, v94, v103, s56
	v_fma_f32 v101, v99, v103, s56
	s_and_b64 s[72:73], s[64:65], s[66:67]
	s_and_b64 s[74:75], s[68:69], s[70:71]
	s_and_b64 s[72:73], s[72:73], s[74:75]
	v_fma_f32 v86, v84, v86, s57
	v_fma_f32 v91, v89, v91, s57
	v_fma_f32 v96, v94, v96, s57
	v_fma_f32 v101, v99, v101, s57
	v_fma_f32 v86, v84, v86, s58
	v_fma_f32 v91, v89, v91, s58
	v_fma_f32 v96, v94, v96, s58
	v_fma_f32 v101, v99, v101, s58
	v_fma_f32 v86, v84, v86, s59
	v_fma_f32 v91, v89, v91, s59
	v_fma_f32 v96, v94, v96, s59
	v_fma_f32 v101, v99, v101, s59
	v_fma_f32 v86, v84, v86, s60
	v_fma_f32 v91, v89, v91, s60
	v_fma_f32 v96, v94, v96, s60
	v_fma_f32 v101, v99, v101, s60
	v_fma_f32 v86, |v82|, v86, |v82|
	v_fma_f32 v91, |v87|, v91, |v87|
	v_fma_f32 v96, |v92|, v96, |v92|
	v_fma_f32 v101, |v97|, v101, |v97|
	s_cmp_eq_u64 s[72:73], exec
	s_cbranch_scc1 .Lgsk_g3_7
	v_fma_f32 v85, |v82|, v102, s50
	v_fma_f32 v90, |v87|, v102, s50
	v_fma_f32 v95, |v92|, v102, s50
	v_fma_f32 v100, |v97|, v102, s50
	v_fma_f32 v85, |v82|, v85, s51
	v_fma_f32 v90, |v87|, v90, s51
	v_fma_f32 v95, |v92|, v95, s51
	v_fma_f32 v100, |v97|, v100, s51
	v_fma_f32 v85, |v82|, v85, s52
	v_fma_f32 v90, |v87|, v90, s52
	v_fma_f32 v95, |v92|, v95, s52
	v_fma_f32 v100, |v97|, v100, s52
	v_fma_f32 v85, |v82|, v85, s53
	v_fma_f32 v90, |v87|, v90, s53
	v_fma_f32 v95, |v92|, v95, s53
	v_fma_f32 v100, |v97|, v100, s53
	v_fma_f32 v85, |v82|, v85, s54
	v_fma_f32 v90, |v87|, v90, s54
	v_fma_f32 v95, |v92|, v95, s54
	v_fma_f32 v100, |v97|, v100, s54
	v_fma_f32 v85, |v82|, v85, s55
	v_fma_f32 v90, |v87|, v90, s55
	v_fma_f32 v95, |v92|, v95, s55
	v_fma_f32 v100, |v97|, v100, s55
	v_fma_f32 v85, |v82|, v85, |v82|
	v_fma_f32 v90, |v87|, v90, |v87|
	v_fma_f32 v95, |v92|, v95, |v92|
	v_fma_f32 v100, |v97|, v100, |v97|
	v_mul_f32_e32 v85, 0xbfb8aa3b, v85
	v_mul_f32_e32 v90, 0xbfb8aa3b, v90
	v_mul_f32_e32 v95, 0xbfb8aa3b, v95
	v_mul_f32_e32 v100, 0xbfb8aa3b, v100
	v_exp_f32_e32 v85, v85
	v_exp_f32_e32 v90, v90
	v_exp_f32_e32 v95, v95
	v_exp_f32_e32 v100, v100
	s_nop 0
	v_sub_f32_e32 v85, 1.0, v85
	v_sub_f32_e32 v90, 1.0, v90
	v_sub_f32_e32 v95, 1.0, v95
	v_sub_f32_e32 v100, 1.0, v100
	v_cndmask_b32_e64 v86, v85, v86, s[64:65]
	v_cndmask_b32_e64 v91, v90, v91, s[66:67]
	v_cndmask_b32_e64 v96, v95, v96, s[68:69]
	v_cndmask_b32_e64 v101, v100, v101, s[70:71]
.Lgsk_g3_7:
	v_fma_f32 v83, |v83|, v86, v83
	v_fma_f32 v88, |v88|, v91, v88
	v_fma_f32 v93, |v93|, v96, v93
	v_fma_f32 v98, |v98|, v101, v98
	v_cvt_f16_f32_e32 v82, v83
	v_cvt_f16_f32_e32 v87, v88
	v_cvt_f16_f32_e32 v92, v93
	v_cvt_f16_f32_e32 v97, v98
	v_cvt_f32_f16_e32 v84, v82
	v_cvt_f32_f16_e32 v89, v87
	v_cvt_f32_f16_e32 v94, v92
	v_cvt_f32_f16_e32 v99, v97
	v_sub_f32_e32 v84, v83, v84
	v_sub_f32_e32 v89, v88, v89
	v_sub_f32_e32 v94, v93, v94
	v_sub_f32_e32 v99, v98, v99
	v_cvt_f16_f32_e32 v84, v84
	v_cvt_f16_f32_e32 v89, v89
	v_cvt_f16_f32_e32 v94, v94
	v_cvt_f16_f32_e32 v99, v99
	ds_write_b16 v71, v82 offset:2400
	ds_write_b16 v71, v87 offset:2544
	ds_write_b16 v71, v92 offset:2688
	ds_write_b16 v71, v97 offset:2832
	ds_write_b16 v71, v84 offset:7008
	ds_write_b16 v71, v89 offset:7152
	ds_write_b16 v71, v94 offset:7296
	ds_write_b16 v71, v99 offset:7440
	ds_read_b128 v[104:107], v74
	ds_read_b128 v[108:111], v74 offset:1152
	ds_read_b128 v[112:115], v74 offset:2304
	ds_read_b128 v[116:119], v74 offset:3456
	ds_read_b128 v[120:123], v74 offset:4608
	ds_read_b128 v[124:127], v74 offset:5760
	ds_read_b128 v[128:131], v74 offset:6912
	ds_read_b128 v[132:135], v74 offset:8064
	v_fma_f32 v82, v30, s61, v140
	v_fma_f32 v87, v31, s61, v140
	v_fma_f32 v92, v32, s61, v140
	v_fma_f32 v97, v33, s61, v140
	v_fma_f32 v83, v30, s62, v144
	v_fma_f32 v88, v31, s62, v144
	v_fma_f32 v93, v32, s62, v144
	v_fma_f32 v98, v33, s62, v144
	v_mul_f32_e32 v84, v82, v82
	v_mul_f32_e32 v89, v87, v87
	v_mul_f32_e32 v94, v92, v92
	v_mul_f32_e32 v99, v97, v97
	v_cmp_lt_f32_e64 s[64:65], |v82|, 1.0
	v_cmp_lt_f32_e64 s[66:67], |v87|, 1.0
	v_cmp_lt_f32_e64 s[68:69], |v92|, 1.0
	v_cmp_lt_f32_e64 s[70:71], |v97|, 1.0
	v_fma_f32 v86, v84, v103, s56
	v_fma_f32 v91, v89, v103, s56
	v_fma_f32 v96, v94, v103, s56
	v_fma_f32 v101, v99, v103, s56
	s_and_b64 s[72:73], s[64:65], s[66:67]
	s_and_b64 s[74:75], s[68:69], s[70:71]
	s_and_b64 s[72:73], s[72:73], s[74:75]
	v_fma_f32 v86, v84, v86, s57
	v_fma_f32 v91, v89, v91, s57
	v_fma_f32 v96, v94, v96, s57
	v_fma_f32 v101, v99, v101, s57
	v_fma_f32 v86, v84, v86, s58
	v_fma_f32 v91, v89, v91, s58
	v_fma_f32 v96, v94, v96, s58
	v_fma_f32 v101, v99, v101, s58
	v_fma_f32 v86, v84, v86, s59
	v_fma_f32 v91, v89, v91, s59
	v_fma_f32 v96, v94, v96, s59
	v_fma_f32 v101, v99, v101, s59
	v_fma_f32 v86, v84, v86, s60
	v_fma_f32 v91, v89, v91, s60
	v_fma_f32 v96, v94, v96, s60
	v_fma_f32 v101, v99, v101, s60
	v_fma_f32 v86, |v82|, v86, |v82|
	v_fma_f32 v91, |v87|, v91, |v87|
	v_fma_f32 v96, |v92|, v96, |v92|
	v_fma_f32 v101, |v97|, v101, |v97|
	s_cmp_eq_u64 s[72:73], exec
	s_cbranch_scc1 .Lgsk_g3_8
	v_fma_f32 v85, |v82|, v102, s50
	v_fma_f32 v90, |v87|, v102, s50
	v_fma_f32 v95, |v92|, v102, s50
	v_fma_f32 v100, |v97|, v102, s50
	v_fma_f32 v85, |v82|, v85, s51
	v_fma_f32 v90, |v87|, v90, s51
	v_fma_f32 v95, |v92|, v95, s51
	v_fma_f32 v100, |v97|, v100, s51
	v_fma_f32 v85, |v82|, v85, s52
	v_fma_f32 v90, |v87|, v90, s52
	v_fma_f32 v95, |v92|, v95, s52
	v_fma_f32 v100, |v97|, v100, s52
	v_fma_f32 v85, |v82|, v85, s53
	v_fma_f32 v90, |v87|, v90, s53
	v_fma_f32 v95, |v92|, v95, s53
	v_fma_f32 v100, |v97|, v100, s53
	v_fma_f32 v85, |v82|, v85, s54
	v_fma_f32 v90, |v87|, v90, s54
	v_fma_f32 v95, |v92|, v95, s54
	v_fma_f32 v100, |v97|, v100, s54
	v_fma_f32 v85, |v82|, v85, s55
	v_fma_f32 v90, |v87|, v90, s55
	v_fma_f32 v95, |v92|, v95, s55
	v_fma_f32 v100, |v97|, v100, s55
	v_fma_f32 v85, |v82|, v85, |v82|
	v_fma_f32 v90, |v87|, v90, |v87|
	v_fma_f32 v95, |v92|, v95, |v92|
	v_fma_f32 v100, |v97|, v100, |v97|
	v_mul_f32_e32 v85, 0xbfb8aa3b, v85
	v_mul_f32_e32 v90, 0xbfb8aa3b, v90
	v_mul_f32_e32 v95, 0xbfb8aa3b, v95
	v_mul_f32_e32 v100, 0xbfb8aa3b, v100
	v_exp_f32_e32 v85, v85
	v_exp_f32_e32 v90, v90
	v_exp_f32_e32 v95, v95
	v_exp_f32_e32 v100, v100
	s_nop 0
	v_sub_f32_e32 v85, 1.0, v85
	v_sub_f32_e32 v90, 1.0, v90
	v_sub_f32_e32 v95, 1.0, v95
	v_sub_f32_e32 v100, 1.0, v100
	v_cndmask_b32_e64 v86, v85, v86, s[64:65]
	v_cndmask_b32_e64 v91, v90, v91, s[66:67]
	v_cndmask_b32_e64 v96, v95, v96, s[68:69]
	v_cndmask_b32_e64 v101, v100, v101, s[70:71]
.Lgsk_g3_8:
	v_fma_f32 v83, |v83|, v86, v83
	v_fma_f32 v88, |v88|, v91, v88
	v_fma_f32 v93, |v93|, v96, v93
	v_fma_f32 v98, |v98|, v101, v98
	v_cvt_f16_f32_e32 v82, v83
	v_cvt_f16_f32_e32 v87, v88
	v_cvt_f16_f32_e32 v92, v93
	v_cvt_f16_f32_e32 v97, v98
	v_cvt_f32_f16_e32 v84, v82
	v_cvt_f32_f16_e32 v89, v87
	v_cvt_f32_f16_e32 v94, v92
	v_cvt_f32_f16_e32 v99, v97
	v_sub_f32_e32 v84, v83, v84
	v_sub_f32_e32 v89, v88, v89
	v_sub_f32_e32 v94, v93, v94
	v_sub_f32_e32 v99, v98, v99
	v_cvt_f16_f32_e32 v84, v84
	v_cvt_f16_f32_e32 v89, v89
	v_cvt_f16_f32_e32 v94, v94
	v_cvt_f16_f32_e32 v99, v99
	s_waitcnt lgkmcnt(0)
	s_sub_i32 s2, s42, 0
	v_cmp_gt_i32_e32 vcc, s2, v75
	s_and_saveexec_b64 s[44:45], vcc
	s_add_u32 s2, s38, 0x0
	s_addc_u32 s3, s39, 0
	global_store_dwordx4 v76, v[104:107], s[2:3]
	s_add_u32 s2, s40, 0x0
	s_addc_u32 s3, s41, 0
	global_store_dwordx4 v76, v[120:123], s[2:3]
	s_mov_b64 exec, s[44:45]
	s_sub_i32 s2, s42, 8
	v_cmp_gt_i32_e32 vcc, s2, v75
	s_and_saveexec_b64 s[44:45], vcc
	s_add_u32 s2, s38, 0x8000
	s_addc_u32 s3, s39, 0
	global_store_dwordx4 v76, v[108:111], s[2:3]
	s_add_u32 s2, s40, 0x8000
	s_addc_u32 s3, s41, 0
	global_store_dwordx4 v76, v[124:127], s[2:3]
	s_mov_b64 exec, s[44:45]
	s_sub_i32 s2, s42, 16
	v_cmp_gt_i32_e32 vcc, s2, v75
	s_and_saveexec_b64 s[44:45], vcc
	s_add_u32 s2, s38, 0x10000
	s_addc_u32 s3, s39, 0
	global_store_dwordx4 v76, v[112:115], s[2:3]
	s_add_u32 s2, s40, 0x10000
	s_addc_u32 s3, s41, 0
	global_store_dwordx4 v76, v[128:131], s[2:3]
	s_mov_b64 exec, s[44:45]
	s_sub_i32 s2, s42, 24
	v_cmp_gt_i32_e32 vcc, s2, v75
	s_and_saveexec_b64 s[44:45], vcc
	s_add_u32 s2, s38, 0x18000
	s_addc_u32 s3, s39, 0
	global_store_dwordx4 v76, v[116:119], s[2:3]
	s_add_u32 s2, s40, 0x18000
	s_addc_u32 s3, s41, 0
	global_store_dwordx4 v76, v[132:135], s[2:3]
	s_mov_b64 exec, s[44:45]
	ds_write_b16 v71, v82
	ds_write_b16 v71, v87 offset:144
	ds_write_b16 v71, v92 offset:288
	ds_write_b16 v71, v97 offset:432
	ds_write_b16 v71, v84 offset:4608
	ds_write_b16 v71, v89 offset:4752
	ds_write_b16 v71, v94 offset:4896
	ds_write_b16 v71, v99 offset:5040
	v_fma_f32 v82, v26, s61, v141
	v_fma_f32 v87, v27, s61, v141
	v_fma_f32 v92, v28, s61, v141
	v_fma_f32 v97, v29, s61, v141
	v_fma_f32 v83, v26, s62, v145
	v_fma_f32 v88, v27, s62, v145
	v_fma_f32 v93, v28, s62, v145
	v_fma_f32 v98, v29, s62, v145
	v_mul_f32_e32 v84, v82, v82
	v_mul_f32_e32 v89, v87, v87
	v_mul_f32_e32 v94, v92, v92
	v_mul_f32_e32 v99, v97, v97
	v_cmp_lt_f32_e64 s[64:65], |v82|, 1.0
	v_cmp_lt_f32_e64 s[66:67], |v87|, 1.0
	v_cmp_lt_f32_e64 s[68:69], |v92|, 1.0
	v_cmp_lt_f32_e64 s[70:71], |v97|, 1.0
	v_fma_f32 v86, v84, v103, s56
	v_fma_f32 v91, v89, v103, s56
	v_fma_f32 v96, v94, v103, s56
	v_fma_f32 v101, v99, v103, s56
	s_and_b64 s[72:73], s[64:65], s[66:67]
	s_and_b64 s[74:75], s[68:69], s[70:71]
	s_and_b64 s[72:73], s[72:73], s[74:75]
	v_fma_f32 v86, v84, v86, s57
	v_fma_f32 v91, v89, v91, s57
	v_fma_f32 v96, v94, v96, s57
	v_fma_f32 v101, v99, v101, s57
	v_fma_f32 v86, v84, v86, s58
	v_fma_f32 v91, v89, v91, s58
	v_fma_f32 v96, v94, v96, s58
	v_fma_f32 v101, v99, v101, s58
	v_fma_f32 v86, v84, v86, s59
	v_fma_f32 v91, v89, v91, s59
	v_fma_f32 v96, v94, v96, s59
	v_fma_f32 v101, v99, v101, s59
	v_fma_f32 v86, v84, v86, s60
	v_fma_f32 v91, v89, v91, s60
	v_fma_f32 v96, v94, v96, s60
	v_fma_f32 v101, v99, v101, s60
	v_fma_f32 v86, |v82|, v86, |v82|
	v_fma_f32 v91, |v87|, v91, |v87|
	v_fma_f32 v96, |v92|, v96, |v92|
	v_fma_f32 v101, |v97|, v101, |v97|
	s_cmp_eq_u64 s[72:73], exec
	s_cbranch_scc1 .Lgsk_g3_9
	v_fma_f32 v85, |v82|, v102, s50
	v_fma_f32 v90, |v87|, v102, s50
	v_fma_f32 v95, |v92|, v102, s50
	v_fma_f32 v100, |v97|, v102, s50
	v_fma_f32 v85, |v82|, v85, s51
	v_fma_f32 v90, |v87|, v90, s51
	v_fma_f32 v95, |v92|, v95, s51
	v_fma_f32 v100, |v97|, v100, s51
	v_fma_f32 v85, |v82|, v85, s52
	v_fma_f32 v90, |v87|, v90, s52
	v_fma_f32 v95, |v92|, v95, s52
	v_fma_f32 v100, |v97|, v100, s52
	v_fma_f32 v85, |v82|, v85, s53
	v_fma_f32 v90, |v87|, v90, s53
	v_fma_f32 v95, |v92|, v95, s53
	v_fma_f32 v100, |v97|, v100, s53
	v_fma_f32 v85, |v82|, v85, s54
	v_fma_f32 v90, |v87|, v90, s54
	v_fma_f32 v95, |v92|, v95, s54
	v_fma_f32 v100, |v97|, v100, s54
	v_fma_f32 v85, |v82|, v85, s55
	v_fma_f32 v90, |v87|, v90, s55
	v_fma_f32 v95, |v92|, v95, s55
	v_fma_f32 v100, |v97|, v100, s55
	v_fma_f32 v85, |v82|, v85, |v82|
	v_fma_f32 v90, |v87|, v90, |v87|
	v_fma_f32 v95, |v92|, v95, |v92|
	v_fma_f32 v100, |v97|, v100, |v97|
	v_mul_f32_e32 v85, 0xbfb8aa3b, v85
	v_mul_f32_e32 v90, 0xbfb8aa3b, v90
	v_mul_f32_e32 v95, 0xbfb8aa3b, v95
	v_mul_f32_e32 v100, 0xbfb8aa3b, v100
	v_exp_f32_e32 v85, v85
	v_exp_f32_e32 v90, v90
	v_exp_f32_e32 v95, v95
	v_exp_f32_e32 v100, v100
	s_nop 0
	v_sub_f32_e32 v85, 1.0, v85
	v_sub_f32_e32 v90, 1.0, v90
	v_sub_f32_e32 v95, 1.0, v95
	v_sub_f32_e32 v100, 1.0, v100
	v_cndmask_b32_e64 v86, v85, v86, s[64:65]
	v_cndmask_b32_e64 v91, v90, v91, s[66:67]
	v_cndmask_b32_e64 v96, v95, v96, s[68:69]
	v_cndmask_b32_e64 v101, v100, v101, s[70:71]
.Lgsk_g3_9:
	v_fma_f32 v83, |v83|, v86, v83
	v_fma_f32 v88, |v88|, v91, v88
	v_fma_f32 v93, |v93|, v96, v93
	v_fma_f32 v98, |v98|, v101, v98
	v_cvt_f16_f32_e32 v82, v83
	v_cvt_f16_f32_e32 v87, v88
	v_cvt_f16_f32_e32 v92, v93
	v_cvt_f16_f32_e32 v97, v98
	v_cvt_f32_f16_e32 v84, v82
	v_cvt_f32_f16_e32 v89, v87
	v_cvt_f32_f16_e32 v94, v92
	v_cvt_f32_f16_e32 v99, v97
	v_sub_f32_e32 v84, v83, v84
	v_sub_f32_e32 v89, v88, v89
	v_sub_f32_e32 v94, v93, v94
	v_sub_f32_e32 v99, v98, v99
	v_cvt_f16_f32_e32 v84, v84
	v_cvt_f16_f32_e32 v89, v89
	v_cvt_f16_f32_e32 v94, v94
	v_cvt_f16_f32_e32 v99, v99
	ds_write_b16 v71, v82 offset:32
	ds_write_b16 v71, v87 offset:176
	ds_write_b16 v71, v92 offset:320
	ds_write_b16 v71, v97 offset:464
	ds_write_b16 v71, v84 offset:4640
	ds_write_b16 v71, v89 offset:4784
	ds_write_b16 v71, v94 offset:4928
	ds_write_b16 v71, v99 offset:5072
	v_fma_f32 v82, v22, s61, v142
	v_fma_f32 v87, v23, s61, v142
	v_fma_f32 v92, v24, s61, v142
	v_fma_f32 v97, v25, s61, v142
	v_fma_f32 v83, v22, s62, v146
	v_fma_f32 v88, v23, s62, v146
	v_fma_f32 v93, v24, s62, v146
	v_fma_f32 v98, v25, s62, v146
	v_mul_f32_e32 v84, v82, v82
	v_mul_f32_e32 v89, v87, v87
	v_mul_f32_e32 v94, v92, v92
	v_mul_f32_e32 v99, v97, v97
	v_cmp_lt_f32_e64 s[64:65], |v82|, 1.0
	v_cmp_lt_f32_e64 s[66:67], |v87|, 1.0
	v_cmp_lt_f32_e64 s[68:69], |v92|, 1.0
	v_cmp_lt_f32_e64 s[70:71], |v97|, 1.0
	v_fma_f32 v86, v84, v103, s56
	v_fma_f32 v91, v89, v103, s56
	v_fma_f32 v96, v94, v103, s56
	v_fma_f32 v101, v99, v103, s56
	s_and_b64 s[72:73], s[64:65], s[66:67]
	s_and_b64 s[74:75], s[68:69], s[70:71]
	s_and_b64 s[72:73], s[72:73], s[74:75]
	v_fma_f32 v86, v84, v86, s57
	v_fma_f32 v91, v89, v91, s57
	v_fma_f32 v96, v94, v96, s57
	v_fma_f32 v101, v99, v101, s57
	v_fma_f32 v86, v84, v86, s58
	v_fma_f32 v91, v89, v91, s58
	v_fma_f32 v96, v94, v96, s58
	v_fma_f32 v101, v99, v101, s58
	v_fma_f32 v86, v84, v86, s59
	v_fma_f32 v91, v89, v91, s59
	v_fma_f32 v96, v94, v96, s59
	v_fma_f32 v101, v99, v101, s59
	v_fma_f32 v86, v84, v86, s60
	v_fma_f32 v91, v89, v91, s60
	v_fma_f32 v96, v94, v96, s60
	v_fma_f32 v101, v99, v101, s60
	v_fma_f32 v86, |v82|, v86, |v82|
	v_fma_f32 v91, |v87|, v91, |v87|
	v_fma_f32 v96, |v92|, v96, |v92|
	v_fma_f32 v101, |v97|, v101, |v97|
	s_cmp_eq_u64 s[72:73], exec
	s_cbranch_scc1 .Lgsk_g3_10
	v_fma_f32 v85, |v82|, v102, s50
	v_fma_f32 v90, |v87|, v102, s50
	v_fma_f32 v95, |v92|, v102, s50
	v_fma_f32 v100, |v97|, v102, s50
	v_fma_f32 v85, |v82|, v85, s51
	v_fma_f32 v90, |v87|, v90, s51
	v_fma_f32 v95, |v92|, v95, s51
	v_fma_f32 v100, |v97|, v100, s51
	v_fma_f32 v85, |v82|, v85, s52
	v_fma_f32 v90, |v87|, v90, s52
	v_fma_f32 v95, |v92|, v95, s52
	v_fma_f32 v100, |v97|, v100, s52
	v_fma_f32 v85, |v82|, v85, s53
	v_fma_f32 v90, |v87|, v90, s53
	v_fma_f32 v95, |v92|, v95, s53
	v_fma_f32 v100, |v97|, v100, s53
	v_fma_f32 v85, |v82|, v85, s54
	v_fma_f32 v90, |v87|, v90, s54
	v_fma_f32 v95, |v92|, v95, s54
	v_fma_f32 v100, |v97|, v100, s54
	v_fma_f32 v85, |v82|, v85, s55
	v_fma_f32 v90, |v87|, v90, s55
	v_fma_f32 v95, |v92|, v95, s55
	v_fma_f32 v100, |v97|, v100, s55
	v_fma_f32 v85, |v82|, v85, |v82|
	v_fma_f32 v90, |v87|, v90, |v87|
	v_fma_f32 v95, |v92|, v95, |v92|
	v_fma_f32 v100, |v97|, v100, |v97|
	v_mul_f32_e32 v85, 0xbfb8aa3b, v85
	v_mul_f32_e32 v90, 0xbfb8aa3b, v90
	v_mul_f32_e32 v95, 0xbfb8aa3b, v95
	v_mul_f32_e32 v100, 0xbfb8aa3b, v100
	v_exp_f32_e32 v85, v85
	v_exp_f32_e32 v90, v90
	v_exp_f32_e32 v95, v95
	v_exp_f32_e32 v100, v100
	s_nop 0
	v_sub_f32_e32 v85, 1.0, v85
	v_sub_f32_e32 v90, 1.0, v90
	v_sub_f32_e32 v95, 1.0, v95
	v_sub_f32_e32 v100, 1.0, v100
	v_cndmask_b32_e64 v86, v85, v86, s[64:65]
	v_cndmask_b32_e64 v91, v90, v91, s[66:67]
	v_cndmask_b32_e64 v96, v95, v96, s[68:69]
	v_cndmask_b32_e64 v101, v100, v101, s[70:71]
.Lgsk_g3_10:
	v_fma_f32 v83, |v83|, v86, v83
	v_fma_f32 v88, |v88|, v91, v88
	v_fma_f32 v93, |v93|, v96, v93
	v_fma_f32 v98, |v98|, v101, v98
	v_cvt_f16_f32_e32 v82, v83
	v_cvt_f16_f32_e32 v87, v88
	v_cvt_f16_f32_e32 v92, v93
	v_cvt_f16_f32_e32 v97, v98
	v_cvt_f32_f16_e32 v84, v82
	v_cvt_f32_f16_e32 v89, v87
	v_cvt_f32_f16_e32 v94, v92
	v_cvt_f32_f16_e32 v99, v97
	v_sub_f32_e32 v84, v83, v84
	v_sub_f32_e32 v89, v88, v89
	v_sub_f32_e32 v94, v93, v94
	v_sub_f32_e32 v99, v98, v99
	v_cvt_f16_f32_e32 v84, v84
	v_cvt_f16_f32_e32 v89, v89
	v_cvt_f16_f32_e32 v94, v94
	v_cvt_f16_f32_e32 v99, v99
	ds_write_b16 v71, v82 offset:64
	ds_write_b16 v71, v87 offset:208
	ds_write_b16 v71, v92 offset:352
	ds_write_b16 v71, v97 offset:496
	ds_write_b16 v71, v84 offset:4672
	ds_write_b16 v71, v89 offset:4816
	ds_write_b16 v71, v94 offset:4960
	ds_write_b16 v71, v99 offset:5104
	v_fma_f32 v82, v18, s61, v143
	v_fma_f32 v87, v19, s61, v143
	v_fma_f32 v92, v20, s61, v143
	v_fma_f32 v97, v21, s61, v143
	v_fma_f32 v83, v18, s62, v147
	v_fma_f32 v88, v19, s62, v147
	v_fma_f32 v93, v20, s62, v147
	v_fma_f32 v98, v21, s62, v147
	v_mul_f32_e32 v84, v82, v82
	v_mul_f32_e32 v89, v87, v87
	v_mul_f32_e32 v94, v92, v92
	v_mul_f32_e32 v99, v97, v97
	v_cmp_lt_f32_e64 s[64:65], |v82|, 1.0
	v_cmp_lt_f32_e64 s[66:67], |v87|, 1.0
	v_cmp_lt_f32_e64 s[68:69], |v92|, 1.0
	v_cmp_lt_f32_e64 s[70:71], |v97|, 1.0
	v_fma_f32 v86, v84, v103, s56
	v_fma_f32 v91, v89, v103, s56
	v_fma_f32 v96, v94, v103, s56
	v_fma_f32 v101, v99, v103, s56
	s_and_b64 s[72:73], s[64:65], s[66:67]
	s_and_b64 s[74:75], s[68:69], s[70:71]
	s_and_b64 s[72:73], s[72:73], s[74:75]
	v_fma_f32 v86, v84, v86, s57
	v_fma_f32 v91, v89, v91, s57
	v_fma_f32 v96, v94, v96, s57
	v_fma_f32 v101, v99, v101, s57
	v_fma_f32 v86, v84, v86, s58
	v_fma_f32 v91, v89, v91, s58
	v_fma_f32 v96, v94, v96, s58
	v_fma_f32 v101, v99, v101, s58
	v_fma_f32 v86, v84, v86, s59
	v_fma_f32 v91, v89, v91, s59
	v_fma_f32 v96, v94, v96, s59
	v_fma_f32 v101, v99, v101, s59
	v_fma_f32 v86, v84, v86, s60
	v_fma_f32 v91, v89, v91, s60
	v_fma_f32 v96, v94, v96, s60
	v_fma_f32 v101, v99, v101, s60
	v_fma_f32 v86, |v82|, v86, |v82|
	v_fma_f32 v91, |v87|, v91, |v87|
	v_fma_f32 v96, |v92|, v96, |v92|
	v_fma_f32 v101, |v97|, v101, |v97|
	s_cmp_eq_u64 s[72:73], exec
	s_cbranch_scc1 .Lgsk_g3_11
	v_fma_f32 v85, |v82|, v102, s50
	v_fma_f32 v90, |v87|, v102, s50
	v_fma_f32 v95, |v92|, v102, s50
	v_fma_f32 v100, |v97|, v102, s50
	v_fma_f32 v85, |v82|, v85, s51
	v_fma_f32 v90, |v87|, v90, s51
	v_fma_f32 v95, |v92|, v95, s51
	v_fma_f32 v100, |v97|, v100, s51
	v_fma_f32 v85, |v82|, v85, s52
	v_fma_f32 v90, |v87|, v90, s52
	v_fma_f32 v95, |v92|, v95, s52
	v_fma_f32 v100, |v97|, v100, s52
	v_fma_f32 v85, |v82|, v85, s53
	v_fma_f32 v90, |v87|, v90, s53
	v_fma_f32 v95, |v92|, v95, s53
	v_fma_f32 v100, |v97|, v100, s53
	v_fma_f32 v85, |v82|, v85, s54
	v_fma_f32 v90, |v87|, v90, s54
	v_fma_f32 v95, |v92|, v95, s54
	v_fma_f32 v100, |v97|, v100, s54
	v_fma_f32 v85, |v82|, v85, s55
	v_fma_f32 v90, |v87|, v90, s55
	v_fma_f32 v95, |v92|, v95, s55
	v_fma_f32 v100, |v97|, v100, s55
	v_fma_f32 v85, |v82|, v85, |v82|
	v_fma_f32 v90, |v87|, v90, |v87|
	v_fma_f32 v95, |v92|, v95, |v92|
	v_fma_f32 v100, |v97|, v100, |v97|
	v_mul_f32_e32 v85, 0xbfb8aa3b, v85
	v_mul_f32_e32 v90, 0xbfb8aa3b, v90
	v_mul_f32_e32 v95, 0xbfb8aa3b, v95
	v_mul_f32_e32 v100, 0xbfb8aa3b, v100
	v_exp_f32_e32 v85, v85
	v_exp_f32_e32 v90, v90
	v_exp_f32_e32 v95, v95
	v_exp_f32_e32 v100, v100
	s_nop 0
	v_sub_f32_e32 v85, 1.0, v85
	v_sub_f32_e32 v90, 1.0, v90
	v_sub_f32_e32 v95, 1.0, v95
	v_sub_f32_e32 v100, 1.0, v100
	v_cndmask_b32_e64 v86, v85, v86, s[64:65]
	v_cndmask_b32_e64 v91, v90, v91, s[66:67]
	v_cndmask_b32_e64 v96, v95, v96, s[68:69]
	v_cndmask_b32_e64 v101, v100, v101, s[70:71]
.Lgsk_g3_11:
	v_fma_f32 v83, |v83|, v86, v83
	v_fma_f32 v88, |v88|, v91, v88
	v_fma_f32 v93, |v93|, v96, v93
	v_fma_f32 v98, |v98|, v101, v98
	v_cvt_f16_f32_e32 v82, v83
	v_cvt_f16_f32_e32 v87, v88
	v_cvt_f16_f32_e32 v92, v93
	v_cvt_f16_f32_e32 v97, v98
	v_cvt_f32_f16_e32 v84, v82
	v_cvt_f32_f16_e32 v89, v87
	v_cvt_f32_f16_e32 v94, v92
	v_cvt_f32_f16_e32 v99, v97
	v_sub_f32_e32 v84, v83, v84
	v_sub_f32_e32 v89, v88, v89
	v_sub_f32_e32 v94, v93, v94
	v_sub_f32_e32 v99, v98, v99
	v_cvt_f16_f32_e32 v84, v84
	v_cvt_f16_f32_e32 v89, v89
	v_cvt_f16_f32_e32 v94, v94
	v_cvt_f16_f32_e32 v99, v99
	ds_write_b16 v71, v82 offset:96
	ds_write_b16 v71, v87 offset:240
	ds_write_b16 v71, v92 offset:384
	ds_write_b16 v71, v97 offset:528
	ds_write_b16 v71, v84 offset:4704
	ds_write_b16 v71, v89 offset:4848
	ds_write_b16 v71, v94 offset:4992
	ds_write_b16 v71, v99 offset:5136
	v_fma_f32 v82, v14, s61, v140
	v_fma_f32 v87, v15, s61, v140
	v_fma_f32 v92, v16, s61, v140
	v_fma_f32 v97, v17, s61, v140
	v_fma_f32 v83, v14, s62, v144
	v_fma_f32 v88, v15, s62, v144
	v_fma_f32 v93, v16, s62, v144
	v_fma_f32 v98, v17, s62, v144
	v_mul_f32_e32 v84, v82, v82
	v_mul_f32_e32 v89, v87, v87
	v_mul_f32_e32 v94, v92, v92
	v_mul_f32_e32 v99, v97, v97
	v_cmp_lt_f32_e64 s[64:65], |v82|, 1.0
	v_cmp_lt_f32_e64 s[66:67], |v87|, 1.0
	v_cmp_lt_f32_e64 s[68:69], |v92|, 1.0
	v_cmp_lt_f32_e64 s[70:71], |v97|, 1.0
	v_fma_f32 v86, v84, v103, s56
	v_fma_f32 v91, v89, v103, s56
	v_fma_f32 v96, v94, v103, s56
	v_fma_f32 v101, v99, v103, s56
	s_and_b64 s[72:73], s[64:65], s[66:67]
	s_and_b64 s[74:75], s[68:69], s[70:71]
	s_and_b64 s[72:73], s[72:73], s[74:75]
	v_fma_f32 v86, v84, v86, s57
	v_fma_f32 v91, v89, v91, s57
	v_fma_f32 v96, v94, v96, s57
	v_fma_f32 v101, v99, v101, s57
	v_fma_f32 v86, v84, v86, s58
	v_fma_f32 v91, v89, v91, s58
	v_fma_f32 v96, v94, v96, s58
	v_fma_f32 v101, v99, v101, s58
	v_fma_f32 v86, v84, v86, s59
	v_fma_f32 v91, v89, v91, s59
	v_fma_f32 v96, v94, v96, s59
	v_fma_f32 v101, v99, v101, s59
	v_fma_f32 v86, v84, v86, s60
	v_fma_f32 v91, v89, v91, s60
	v_fma_f32 v96, v94, v96, s60
	v_fma_f32 v101, v99, v101, s60
	v_fma_f32 v86, |v82|, v86, |v82|
	v_fma_f32 v91, |v87|, v91, |v87|
	v_fma_f32 v96, |v92|, v96, |v92|
	v_fma_f32 v101, |v97|, v101, |v97|
	s_cmp_eq_u64 s[72:73], exec
	s_cbranch_scc1 .Lgsk_g3_12
	v_fma_f32 v85, |v82|, v102, s50
	v_fma_f32 v90, |v87|, v102, s50
	v_fma_f32 v95, |v92|, v102, s50
	v_fma_f32 v100, |v97|, v102, s50
	v_fma_f32 v85, |v82|, v85, s51
	v_fma_f32 v90, |v87|, v90, s51
	v_fma_f32 v95, |v92|, v95, s51
	v_fma_f32 v100, |v97|, v100, s51
	v_fma_f32 v85, |v82|, v85, s52
	v_fma_f32 v90, |v87|, v90, s52
	v_fma_f32 v95, |v92|, v95, s52
	v_fma_f32 v100, |v97|, v100, s52
	v_fma_f32 v85, |v82|, v85, s53
	v_fma_f32 v90, |v87|, v90, s53
	v_fma_f32 v95, |v92|, v95, s53
	v_fma_f32 v100, |v97|, v100, s53
	v_fma_f32 v85, |v82|, v85, s54
	v_fma_f32 v90, |v87|, v90, s54
	v_fma_f32 v95, |v92|, v95, s54
	v_fma_f32 v100, |v97|, v100, s54
	v_fma_f32 v85, |v82|, v85, s55
	v_fma_f32 v90, |v87|, v90, s55
	v_fma_f32 v95, |v92|, v95, s55
	v_fma_f32 v100, |v97|, v100, s55
	v_fma_f32 v85, |v82|, v85, |v82|
	v_fma_f32 v90, |v87|, v90, |v87|
	v_fma_f32 v95, |v92|, v95, |v92|
	v_fma_f32 v100, |v97|, v100, |v97|
	v_mul_f32_e32 v85, 0xbfb8aa3b, v85
	v_mul_f32_e32 v90, 0xbfb8aa3b, v90
	v_mul_f32_e32 v95, 0xbfb8aa3b, v95
	v_mul_f32_e32 v100, 0xbfb8aa3b, v100
	v_exp_f32_e32 v85, v85
	v_exp_f32_e32 v90, v90
	v_exp_f32_e32 v95, v95
	v_exp_f32_e32 v100, v100
	s_nop 0
	v_sub_f32_e32 v85, 1.0, v85
	v_sub_f32_e32 v90, 1.0, v90
	v_sub_f32_e32 v95, 1.0, v95
	v_sub_f32_e32 v100, 1.0, v100
	v_cndmask_b32_e64 v86, v85, v86, s[64:65]
	v_cndmask_b32_e64 v91, v90, v91, s[66:67]
	v_cndmask_b32_e64 v96, v95, v96, s[68:69]
	v_cndmask_b32_e64 v101, v100, v101, s[70:71]
.Lgsk_g3_12:
	v_fma_f32 v83, |v83|, v86, v83
	v_fma_f32 v88, |v88|, v91, v88
	v_fma_f32 v93, |v93|, v96, v93
	v_fma_f32 v98, |v98|, v101, v98
	v_cvt_f16_f32_e32 v82, v83
	v_cvt_f16_f32_e32 v87, v88
	v_cvt_f16_f32_e32 v92, v93
	v_cvt_f16_f32_e32 v97, v98
	v_cvt_f32_f16_e32 v84, v82
	v_cvt_f32_f16_e32 v89, v87
	v_cvt_f32_f16_e32 v94, v92
	v_cvt_f32_f16_e32 v99, v97
	v_sub_f32_e32 v84, v83, v84
	v_sub_f32_e32 v89, v88, v89
	v_sub_f32_e32 v94, v93, v94
	v_sub_f32_e32 v99, v98, v99
	v_cvt_f16_f32_e32 v84, v84
	v_cvt_f16_f32_e32 v89, v89
	v_cvt_f16_f32_e32 v94, v94
	v_cvt_f16_f32_e32 v99, v99
	ds_write_b16 v71, v82 offset:2304
	ds_write_b16 v71, v87 offset:2448
	ds_write_b16 v71, v92 offset:2592
	ds_write_b16 v71, v97 offset:2736
	ds_write_b16 v71, v84 offset:6912
	ds_write_b16 v71, v89 offset:7056
	ds_write_b16 v71, v94 offset:7200
	ds_write_b16 v71, v99 offset:7344
	v_fma_f32 v82, v10, s61, v141
	v_fma_f32 v87, v11, s61, v141
	v_fma_f32 v92, v12, s61, v141
	v_fma_f32 v97, v13, s61, v141
	v_fma_f32 v83, v10, s62, v145
	v_fma_f32 v88, v11, s62, v145
	v_fma_f32 v93, v12, s62, v145
	v_fma_f32 v98, v13, s62, v145
	v_mul_f32_e32 v84, v82, v82
	v_mul_f32_e32 v89, v87, v87
	v_mul_f32_e32 v94, v92, v92
	v_mul_f32_e32 v99, v97, v97
	v_cmp_lt_f32_e64 s[64:65], |v82|, 1.0
	v_cmp_lt_f32_e64 s[66:67], |v87|, 1.0
	v_cmp_lt_f32_e64 s[68:69], |v92|, 1.0
	v_cmp_lt_f32_e64 s[70:71], |v97|, 1.0
	v_fma_f32 v86, v84, v103, s56
	v_fma_f32 v91, v89, v103, s56
	v_fma_f32 v96, v94, v103, s56
	v_fma_f32 v101, v99, v103, s56
	s_and_b64 s[72:73], s[64:65], s[66:67]
	s_and_b64 s[74:75], s[68:69], s[70:71]
	s_and_b64 s[72:73], s[72:73], s[74:75]
	v_fma_f32 v86, v84, v86, s57
	v_fma_f32 v91, v89, v91, s57
	v_fma_f32 v96, v94, v96, s57
	v_fma_f32 v101, v99, v101, s57
	v_fma_f32 v86, v84, v86, s58
	v_fma_f32 v91, v89, v91, s58
	v_fma_f32 v96, v94, v96, s58
	v_fma_f32 v101, v99, v101, s58
	v_fma_f32 v86, v84, v86, s59
	v_fma_f32 v91, v89, v91, s59
	v_fma_f32 v96, v94, v96, s59
	v_fma_f32 v101, v99, v101, s59
	v_fma_f32 v86, v84, v86, s60
	v_fma_f32 v91, v89, v91, s60
	v_fma_f32 v96, v94, v96, s60
	v_fma_f32 v101, v99, v101, s60
	v_fma_f32 v86, |v82|, v86, |v82|
	v_fma_f32 v91, |v87|, v91, |v87|
	v_fma_f32 v96, |v92|, v96, |v92|
	v_fma_f32 v101, |v97|, v101, |v97|
	s_cmp_eq_u64 s[72:73], exec
	s_cbranch_scc1 .Lgsk_g3_13
	v_fma_f32 v85, |v82|, v102, s50
	v_fma_f32 v90, |v87|, v102, s50
	v_fma_f32 v95, |v92|, v102, s50
	v_fma_f32 v100, |v97|, v102, s50
	v_fma_f32 v85, |v82|, v85, s51
	v_fma_f32 v90, |v87|, v90, s51
	v_fma_f32 v95, |v92|, v95, s51
	v_fma_f32 v100, |v97|, v100, s51
	v_fma_f32 v85, |v82|, v85, s52
	v_fma_f32 v90, |v87|, v90, s52
	v_fma_f32 v95, |v92|, v95, s52
	v_fma_f32 v100, |v97|, v100, s52
	v_fma_f32 v85, |v82|, v85, s53
	v_fma_f32 v90, |v87|, v90, s53
	v_fma_f32 v95, |v92|, v95, s53
	v_fma_f32 v100, |v97|, v100, s53
	v_fma_f32 v85, |v82|, v85, s54
	v_fma_f32 v90, |v87|, v90, s54
	v_fma_f32 v95, |v92|, v95, s54
	v_fma_f32 v100, |v97|, v100, s54
	v_fma_f32 v85, |v82|, v85, s55
	v_fma_f32 v90, |v87|, v90, s55
	v_fma_f32 v95, |v92|, v95, s55
	v_fma_f32 v100, |v97|, v100, s55
	v_fma_f32 v85, |v82|, v85, |v82|
	v_fma_f32 v90, |v87|, v90, |v87|
	v_fma_f32 v95, |v92|, v95, |v92|
	v_fma_f32 v100, |v97|, v100, |v97|
	v_mul_f32_e32 v85, 0xbfb8aa3b, v85
	v_mul_f32_e32 v90, 0xbfb8aa3b, v90
	v_mul_f32_e32 v95, 0xbfb8aa3b, v95
	v_mul_f32_e32 v100, 0xbfb8aa3b, v100
	v_exp_f32_e32 v85, v85
	v_exp_f32_e32 v90, v90
	v_exp_f32_e32 v95, v95
	v_exp_f32_e32 v100, v100
	s_nop 0
	v_sub_f32_e32 v85, 1.0, v85
	v_sub_f32_e32 v90, 1.0, v90
	v_sub_f32_e32 v95, 1.0, v95
	v_sub_f32_e32 v100, 1.0, v100
	v_cndmask_b32_e64 v86, v85, v86, s[64:65]
	v_cndmask_b32_e64 v91, v90, v91, s[66:67]
	v_cndmask_b32_e64 v96, v95, v96, s[68:69]
	v_cndmask_b32_e64 v101, v100, v101, s[70:71]
.Lgsk_g3_13:
	v_fma_f32 v83, |v83|, v86, v83
	v_fma_f32 v88, |v88|, v91, v88
	v_fma_f32 v93, |v93|, v96, v93
	v_fma_f32 v98, |v98|, v101, v98
	v_cvt_f16_f32_e32 v82, v83
	v_cvt_f16_f32_e32 v87, v88
	v_cvt_f16_f32_e32 v92, v93
	v_cvt_f16_f32_e32 v97, v98
	v_cvt_f32_f16_e32 v84, v82
	v_cvt_f32_f16_e32 v89, v87
	v_cvt_f32_f16_e32 v94, v92
	v_cvt_f32_f16_e32 v99, v97
	v_sub_f32_e32 v84, v83, v84
	v_sub_f32_e32 v89, v88, v89
	v_sub_f32_e32 v94, v93, v94
	v_sub_f32_e32 v99, v98, v99
	v_cvt_f16_f32_e32 v84, v84
	v_cvt_f16_f32_e32 v89, v89
	v_cvt_f16_f32_e32 v94, v94
	v_cvt_f16_f32_e32 v99, v99
	ds_write_b16 v71, v82 offset:2336
	ds_write_b16 v71, v87 offset:2480
	ds_write_b16 v71, v92 offset:2624
	ds_write_b16 v71, v97 offset:2768
	ds_write_b16 v71, v84 offset:6944
	ds_write_b16 v71, v89 offset:7088
	ds_write_b16 v71, v94 offset:7232
	ds_write_b16 v71, v99 offset:7376
	v_fma_f32 v82, v6, s61, v142
	v_fma_f32 v87, v7, s61, v142
	v_fma_f32 v92, v8, s61, v142
	v_fma_f32 v97, v9, s61, v142
	v_fma_f32 v83, v6, s62, v146
	v_fma_f32 v88, v7, s62, v146
	v_fma_f32 v93, v8, s62, v146
	v_fma_f32 v98, v9, s62, v146
	v_mul_f32_e32 v84, v82, v82
	v_mul_f32_e32 v89, v87, v87
	v_mul_f32_e32 v94, v92, v92
	v_mul_f32_e32 v99, v97, v97
	v_cmp_lt_f32_e64 s[64:65], |v82|, 1.0
	v_cmp_lt_f32_e64 s[66:67], |v87|, 1.0
	v_cmp_lt_f32_e64 s[68:69], |v92|, 1.0
	v_cmp_lt_f32_e64 s[70:71], |v97|, 1.0
	v_fma_f32 v86, v84, v103, s56
	v_fma_f32 v91, v89, v103, s56
	v_fma_f32 v96, v94, v103, s56
	v_fma_f32 v101, v99, v103, s56
	s_and_b64 s[72:73], s[64:65], s[66:67]
	s_and_b64 s[74:75], s[68:69], s[70:71]
	s_and_b64 s[72:73], s[72:73], s[74:75]
	v_fma_f32 v86, v84, v86, s57
	v_fma_f32 v91, v89, v91, s57
	v_fma_f32 v96, v94, v96, s57
	v_fma_f32 v101, v99, v101, s57
	v_fma_f32 v86, v84, v86, s58
	v_fma_f32 v91, v89, v91, s58
	v_fma_f32 v96, v94, v96, s58
	v_fma_f32 v101, v99, v101, s58
	v_fma_f32 v86, v84, v86, s59
	v_fma_f32 v91, v89, v91, s59
	v_fma_f32 v96, v94, v96, s59
	v_fma_f32 v101, v99, v101, s59
	v_fma_f32 v86, v84, v86, s60
	v_fma_f32 v91, v89, v91, s60
	v_fma_f32 v96, v94, v96, s60
	v_fma_f32 v101, v99, v101, s60
	v_fma_f32 v86, |v82|, v86, |v82|
	v_fma_f32 v91, |v87|, v91, |v87|
	v_fma_f32 v96, |v92|, v96, |v92|
	v_fma_f32 v101, |v97|, v101, |v97|
	s_cmp_eq_u64 s[72:73], exec
	s_cbranch_scc1 .Lgsk_g3_14
	v_fma_f32 v85, |v82|, v102, s50
	v_fma_f32 v90, |v87|, v102, s50
	v_fma_f32 v95, |v92|, v102, s50
	v_fma_f32 v100, |v97|, v102, s50
	v_fma_f32 v85, |v82|, v85, s51
	v_fma_f32 v90, |v87|, v90, s51
	v_fma_f32 v95, |v92|, v95, s51
	v_fma_f32 v100, |v97|, v100, s51
	v_fma_f32 v85, |v82|, v85, s52
	v_fma_f32 v90, |v87|, v90, s52
	v_fma_f32 v95, |v92|, v95, s52
	v_fma_f32 v100, |v97|, v100, s52
	v_fma_f32 v85, |v82|, v85, s53
	v_fma_f32 v90, |v87|, v90, s53
	v_fma_f32 v95, |v92|, v95, s53
	v_fma_f32 v100, |v97|, v100, s53
	v_fma_f32 v85, |v82|, v85, s54
	v_fma_f32 v90, |v87|, v90, s54
	v_fma_f32 v95, |v92|, v95, s54
	v_fma_f32 v100, |v97|, v100, s54
	v_fma_f32 v85, |v82|, v85, s55
	v_fma_f32 v90, |v87|, v90, s55
	v_fma_f32 v95, |v92|, v95, s55
	v_fma_f32 v100, |v97|, v100, s55
	v_fma_f32 v85, |v82|, v85, |v82|
	v_fma_f32 v90, |v87|, v90, |v87|
	v_fma_f32 v95, |v92|, v95, |v92|
	v_fma_f32 v100, |v97|, v100, |v97|
	v_mul_f32_e32 v85, 0xbfb8aa3b, v85
	v_mul_f32_e32 v90, 0xbfb8aa3b, v90
	v_mul_f32_e32 v95, 0xbfb8aa3b, v95
	v_mul_f32_e32 v100, 0xbfb8aa3b, v100
	v_exp_f32_e32 v85, v85
	v_exp_f32_e32 v90, v90
	v_exp_f32_e32 v95, v95
	v_exp_f32_e32 v100, v100
	s_nop 0
	v_sub_f32_e32 v85, 1.0, v85
	v_sub_f32_e32 v90, 1.0, v90
	v_sub_f32_e32 v95, 1.0, v95
	v_sub_f32_e32 v100, 1.0, v100
	v_cndmask_b32_e64 v86, v85, v86, s[64:65]
	v_cndmask_b32_e64 v91, v90, v91, s[66:67]
	v_cndmask_b32_e64 v96, v95, v96, s[68:69]
	v_cndmask_b32_e64 v101, v100, v101, s[70:71]
.Lgsk_g3_14:
	v_fma_f32 v83, |v83|, v86, v83
	v_fma_f32 v88, |v88|, v91, v88
	v_fma_f32 v93, |v93|, v96, v93
	v_fma_f32 v98, |v98|, v101, v98
	v_cvt_f16_f32_e32 v82, v83
	v_cvt_f16_f32_e32 v87, v88
	v_cvt_f16_f32_e32 v92, v93
	v_cvt_f16_f32_e32 v97, v98
	v_cvt_f32_f16_e32 v84, v82
	v_cvt_f32_f16_e32 v89, v87
	v_cvt_f32_f16_e32 v94, v92
	v_cvt_f32_f16_e32 v99, v97
	v_sub_f32_e32 v84, v83, v84
	v_sub_f32_e32 v89, v88, v89
	v_sub_f32_e32 v94, v93, v94
	v_sub_f32_e32 v99, v98, v99
	v_cvt_f16_f32_e32 v84, v84
	v_cvt_f16_f32_e32 v89, v89
	v_cvt_f16_f32_e32 v94, v94
	v_cvt_f16_f32_e32 v99, v99
	ds_write_b16 v71, v82 offset:2368
	ds_write_b16 v71, v87 offset:2512
	ds_write_b16 v71, v92 offset:2656
	ds_write_b16 v71, v97 offset:2800
	ds_write_b16 v71, v84 offset:6976
	ds_write_b16 v71, v89 offset:7120
	ds_write_b16 v71, v94 offset:7264
	ds_write_b16 v71, v99 offset:7408
	v_fma_f32 v82, v2, s61, v143
	v_fma_f32 v87, v3, s61, v143
	v_fma_f32 v92, v4, s61, v143
	v_fma_f32 v97, v5, s61, v143
	v_fma_f32 v83, v2, s62, v147
	v_fma_f32 v88, v3, s62, v147
	v_fma_f32 v93, v4, s62, v147
	v_fma_f32 v98, v5, s62, v147
	v_mul_f32_e32 v84, v82, v82
	v_mul_f32_e32 v89, v87, v87
	v_mul_f32_e32 v94, v92, v92
	v_mul_f32_e32 v99, v97, v97
	v_cmp_lt_f32_e64 s[64:65], |v82|, 1.0
	v_cmp_lt_f32_e64 s[66:67], |v87|, 1.0
	v_cmp_lt_f32_e64 s[68:69], |v92|, 1.0
	v_cmp_lt_f32_e64 s[70:71], |v97|, 1.0
	v_fma_f32 v86, v84, v103, s56
	v_fma_f32 v91, v89, v103, s56
	v_fma_f32 v96, v94, v103, s56
	v_fma_f32 v101, v99, v103, s56
	s_and_b64 s[72:73], s[64:65], s[66:67]
	s_and_b64 s[74:75], s[68:69], s[70:71]
	s_and_b64 s[72:73], s[72:73], s[74:75]
	v_fma_f32 v86, v84, v86, s57
	v_fma_f32 v91, v89, v91, s57
	v_fma_f32 v96, v94, v96, s57
	v_fma_f32 v101, v99, v101, s57
	v_fma_f32 v86, v84, v86, s58
	v_fma_f32 v91, v89, v91, s58
	v_fma_f32 v96, v94, v96, s58
	v_fma_f32 v101, v99, v101, s58
	v_fma_f32 v86, v84, v86, s59
	v_fma_f32 v91, v89, v91, s59
	v_fma_f32 v96, v94, v96, s59
	v_fma_f32 v101, v99, v101, s59
	v_fma_f32 v86, v84, v86, s60
	v_fma_f32 v91, v89, v91, s60
	v_fma_f32 v96, v94, v96, s60
	v_fma_f32 v101, v99, v101, s60
	v_fma_f32 v86, |v82|, v86, |v82|
	v_fma_f32 v91, |v87|, v91, |v87|
	v_fma_f32 v96, |v92|, v96, |v92|
	v_fma_f32 v101, |v97|, v101, |v97|
	s_cmp_eq_u64 s[72:73], exec
	s_cbranch_scc1 .Lgsk_g3_15
	v_fma_f32 v85, |v82|, v102, s50
	v_fma_f32 v90, |v87|, v102, s50
	v_fma_f32 v95, |v92|, v102, s50
	v_fma_f32 v100, |v97|, v102, s50
	v_fma_f32 v85, |v82|, v85, s51
	v_fma_f32 v90, |v87|, v90, s51
	v_fma_f32 v95, |v92|, v95, s51
	v_fma_f32 v100, |v97|, v100, s51
	v_fma_f32 v85, |v82|, v85, s52
	v_fma_f32 v90, |v87|, v90, s52
	v_fma_f32 v95, |v92|, v95, s52
	v_fma_f32 v100, |v97|, v100, s52
	v_fma_f32 v85, |v82|, v85, s53
	v_fma_f32 v90, |v87|, v90, s53
	v_fma_f32 v95, |v92|, v95, s53
	v_fma_f32 v100, |v97|, v100, s53
	v_fma_f32 v85, |v82|, v85, s54
	v_fma_f32 v90, |v87|, v90, s54
	v_fma_f32 v95, |v92|, v95, s54
	v_fma_f32 v100, |v97|, v100, s54
	v_fma_f32 v85, |v82|, v85, s55
	v_fma_f32 v90, |v87|, v90, s55
	v_fma_f32 v95, |v92|, v95, s55
	v_fma_f32 v100, |v97|, v100, s55
	v_fma_f32 v85, |v82|, v85, |v82|
	v_fma_f32 v90, |v87|, v90, |v87|
	v_fma_f32 v95, |v92|, v95, |v92|
	v_fma_f32 v100, |v97|, v100, |v97|
	v_mul_f32_e32 v85, 0xbfb8aa3b, v85
	v_mul_f32_e32 v90, 0xbfb8aa3b, v90
	v_mul_f32_e32 v95, 0xbfb8aa3b, v95
	v_mul_f32_e32 v100, 0xbfb8aa3b, v100
	v_exp_f32_e32 v85, v85
	v_exp_f32_e32 v90, v90
	v_exp_f32_e32 v95, v95
	v_exp_f32_e32 v100, v100
	s_nop 0
	v_sub_f32_e32 v85, 1.0, v85
	v_sub_f32_e32 v90, 1.0, v90
	v_sub_f32_e32 v95, 1.0, v95
	v_sub_f32_e32 v100, 1.0, v100
	v_cndmask_b32_e64 v86, v85, v86, s[64:65]
	v_cndmask_b32_e64 v91, v90, v91, s[66:67]
	v_cndmask_b32_e64 v96, v95, v96, s[68:69]
	v_cndmask_b32_e64 v101, v100, v101, s[70:71]
.Lgsk_g3_15:
	v_fma_f32 v83, |v83|, v86, v83
	v_fma_f32 v88, |v88|, v91, v88
	v_fma_f32 v93, |v93|, v96, v93
	v_fma_f32 v98, |v98|, v101, v98
	v_cvt_f16_f32_e32 v82, v83
	v_cvt_f16_f32_e32 v87, v88
	v_cvt_f16_f32_e32 v92, v93
	v_cvt_f16_f32_e32 v97, v98
	v_cvt_f32_f16_e32 v84, v82
	v_cvt_f32_f16_e32 v89, v87
	v_cvt_f32_f16_e32 v94, v92
	v_cvt_f32_f16_e32 v99, v97
	v_sub_f32_e32 v84, v83, v84
	v_sub_f32_e32 v89, v88, v89
	v_sub_f32_e32 v94, v93, v94
	v_sub_f32_e32 v99, v98, v99
	v_cvt_f16_f32_e32 v84, v84
	v_cvt_f16_f32_e32 v89, v89
	v_cvt_f16_f32_e32 v94, v94
	v_cvt_f16_f32_e32 v99, v99
	ds_write_b16 v71, v82 offset:2400
	ds_write_b16 v71, v87 offset:2544
	ds_write_b16 v71, v92 offset:2688
	ds_write_b16 v71, v97 offset:2832
	ds_write_b16 v71, v84 offset:7008
	ds_write_b16 v71, v89 offset:7152
	ds_write_b16 v71, v94 offset:7296
	ds_write_b16 v71, v99 offset:7440
	ds_read_b128 v[104:107], v74
	ds_read_b128 v[108:111], v74 offset:1152
	ds_read_b128 v[112:115], v74 offset:2304
	ds_read_b128 v[116:119], v74 offset:3456
	ds_read_b128 v[120:123], v74 offset:4608
	ds_read_b128 v[124:127], v74 offset:5760
	ds_read_b128 v[128:131], v74 offset:6912
	ds_read_b128 v[132:135], v74 offset:8064
	s_waitcnt lgkmcnt(0)
	s_sub_i32 s2, s42, 32
	v_cmp_gt_i32_e32 vcc, s2, v75
	s_and_saveexec_b64 s[44:45], vcc
	s_add_u32 s2, s38, 0x20000
	s_addc_u32 s3, s39, 0
	global_store_dwordx4 v76, v[104:107], s[2:3]
	s_add_u32 s2, s40, 0x20000
	s_addc_u32 s3, s41, 0
	global_store_dwordx4 v76, v[120:123], s[2:3]
	s_mov_b64 exec, s[44:45]
	s_sub_i32 s2, s42, 40
	v_cmp_gt_i32_e32 vcc, s2, v75
	s_and_saveexec_b64 s[44:45], vcc
	s_add_u32 s2, s38, 0x28000
	s_addc_u32 s3, s39, 0
	global_store_dwordx4 v76, v[108:111], s[2:3]
	s_add_u32 s2, s40, 0x28000
	s_addc_u32 s3, s41, 0
	global_store_dwordx4 v76, v[124:127], s[2:3]
	s_mov_b64 exec, s[44:45]
	s_sub_i32 s2, s42, 48
	v_cmp_gt_i32_e32 vcc, s2, v75
	s_and_saveexec_b64 s[44:45], vcc
	s_add_u32 s2, s38, 0x30000
	s_addc_u32 s3, s39, 0
	global_store_dwordx4 v76, v[112:115], s[2:3]
	s_add_u32 s2, s40, 0x30000
	s_addc_u32 s3, s41, 0
	global_store_dwordx4 v76, v[128:131], s[2:3]
	s_mov_b64 exec, s[44:45]
	s_sub_i32 s2, s42, 56
	v_cmp_gt_i32_e32 vcc, s2, v75
	s_and_saveexec_b64 s[44:45], vcc
	s_add_u32 s2, s38, 0x38000
	s_addc_u32 s3, s39, 0
	global_store_dwordx4 v76, v[116:119], s[2:3]
	s_add_u32 s2, s40, 0x38000
	s_addc_u32 s3, s41, 0
	global_store_dwordx4 v76, v[132:135], s[2:3]
	s_mov_b64 exec, s[44:45]
	s_endpgm
